# grid barrier thread-0 protocol rewritten by hand: generation tracked in an SGPR (no divisions), last arriver releases all XCD generation words directly (one hop)
# speedup vs baseline: 1.0065x; 1.0065x over previous
; #define LAS __attribute__((address_space(3)))
; __global__ void __launch_bounds__(NTHR, 2) fwd(Args args) {
;     extern __shared__ __attribute__((aligned(16))) unsigned char lds[];
;     Frame F;
;     F.lds = (LAS unsigned char*)lds; F.glds = lds; F.ws = args.ws; F.ctl = (unsigned*)(args.ws + WS_CTL);
;     F.tid = threadIdx.x; F.lane = F.tid & 63; F.wave = __builtin_amdgcn_readfirstlane(F.tid >> 6);
;     F.G = gridDim.x; F.gw = blockIdx.x * NWAVES + F.wave; F.NGW = F.G * NWAVES;
;     volatile LAS unsigned* MISC = (volatile LAS unsigned*)(F.lds + MISC_OFF);
;     for (int u = F.tid; u < (LDS_BYTES - LDSCTL_OFF) / 4; u += NTHR) ((LAS unsigned*)(F.lds + LDSCTL_OFF))[u] = 0u;
;     __syncthreads();
;     if (F.tid < N_INPUTS) { const unsigned long long p = (unsigned long long)args.in[F.tid]; LAS unsigned* t = (LAS unsigned*)(F.lds + PTAB_OFF) + 2 * F.tid; t[0] = (unsigned)p; t[1] = (unsigned)(p >> 32); }
;     __syncthreads();
_Z3fwd4Args:
	s_mov_b32 s101, 0
	s_load_dword s48, s[0:1], 0xd0
	s_add_u32 s4, s0, 0xd0
	v_writelane_b32 v255, s0, 0
	s_addc_u32 s5, s1, 0
	v_lshl_add_u32 v1, v0, 2, 0
	v_writelane_b32 v255, s1, 1
	v_writelane_b32 v255, s4, 2
	v_add_u32_e32 v1, 0x20000, v1
	v_mov_b32_e32 v2, 0
	v_readfirstlane_b32 s54, v0
	v_writelane_b32 v255, s5, 3
	ds_write2st64_b32 v1, v2, v2 offset1:8
	ds_write2st64_b32 v1, v2, v2 offset0:16 offset1:24
	v_or_b32_e32 v1, 0x800, v0
	s_mov_b64 s[0:1], -1
	s_and_saveexec_b64 s[4:5], s[0:1]
	v_lshl_add_u32 v3, v1, 2, 0
	v_add_u32_e32 v3, 0x20000, v3
	ds_write_b32 v3, v2
	s_or_b64 exec, exec, s[4:5]
	s_and_saveexec_b64 s[4:5], s[0:1]
	s_add_i32 s0, 0, 0x20000
	v_lshl_add_u32 v1, v1, 2, s0
	v_mov_b32_e32 v2, 0
	ds_write_b32 v1, v2 offset:2048
	s_or_b64 exec, exec, s[4:5]
	v_or_b32_e32 v1, 0xc00, v0
	v_cmp_gt_u32_e64 s[0:1], 7, 6
	v_cmp_gt_u32_e64 s[6:7], 7, 5
	s_and_saveexec_b64 s[4:5], s[6:7]
	v_lshl_add_u32 v2, v1, 2, 0
	v_add_u32_e32 v2, 0x20000, v2
	v_mov_b32_e32 v3, 0
	ds_write_b32 v2, v3
	s_or_b64 exec, exec, s[4:5]
	v_readlane_b32 s4, v255, 0
	v_readlane_b32 s5, v255, 1
	s_load_dwordx2 s[50:51], s[4:5], 0xc0
	s_and_saveexec_b64 s[4:5], s[0:1]
	s_add_i32 s0, 0, 0x20000
	v_lshl_add_u32 v1, v1, 2, s0
	v_mov_b32_e32 v2, 0
	ds_write_b32 v1, v2 offset:2048
	s_or_b64 exec, exec, s[4:5]
	v_cmp_gt_u32_e32 vcc, 23, v0
	s_waitcnt lgkmcnt(0)
	s_barrier
	s_and_saveexec_b64 s[0:1], vcc
	s_cbranch_execz .LBB0_10
	v_readlane_b32 s4, v255, 0
	v_lshlrev_b32_e32 v1, 3, v0
	v_readlane_b32 s5, v255, 1
	s_nop 4
	global_load_dwordx2 v[2:3], v1, s[4:5]
	v_add_u32_e32 v1, 0, v1
	v_add_u32_e32 v1, 0x20200, v1
	s_waitcnt vmcnt(0)
	ds_write_b64 v1, v[2:3]

; __device__ __forceinline__ void xcd_barrier(const XcdBarrier& b) {
;     ...
;     }
;     __syncthreads();
.LBB0_98:
	s_or_b64 exec, exec, s[0:1]
	s_add_u32 s101, s101, 1
	s_waitcnt lgkmcnt(0)
	s_barrier

; __device__ __forceinline__ unsigned xb_ld(unsigned* p)              { return __hip_atomic_load(p, __ATOMIC_RELAXED, __HIP_MEMORY_SCOPE_AGENT); }
; __device__ __forceinline__ unsigned xb_add(unsigned* p, unsigned v) { return __hip_atomic_fetch_add(p, v, __ATOMIC_RELAXED, __HIP_MEMORY_SCOPE_AGENT); }
; #define XB_SPIN(cond, bar) do { unsigned _sp = 0; while (cond) { __builtin_amdgcn_s_sleep(1); \
;     if ((++_sp & 255u) == 0u) { if (xb_ld(&(bar)[XB_TMO])) break; if (_sp > XB_SPIN_CAP) { atomicAdd(&(bar)[XB_TMO], 1u); break; } } } } while (0)
; #define SEAM(k) do { if (IN(k) && IN((k) + 1)) GRID_BAR(); } while (0)
; __device__ __forceinline__ void xcd_barrier(const XcdBarrier& b) {
;     asm volatile("s_waitcnt vmcnt(0)" ::: "memory");
;     __syncthreads();
;     if (threadIdx.x == 0) {
;         unsigned* bar = b.bar;
;         __builtin_amdgcn_s_waitcnt(0);
;         unsigned nloc = b.st[0], nx = b.st[1];
;         if (nloc == 0u) { xcd_barrier_complete(bar, b.x, nloc, nx); b.st[0] = nloc; b.st[1] = nx; }
;         const unsigned old = xb_add(&bar[XB_XSUB(b.x)], 1u);
;         const unsigned gen = old / nloc;
;         if (old + 1u == (gen + 1u) * nloc) {
;             __builtin_amdgcn_fence(__ATOMIC_RELEASE, "agent");
;             asm volatile("s_waitcnt vmcnt(0)" ::: "memory");
;             const unsigned og = xb_add(&bar[XB_TOP], 1u);
;             const unsigned tg = og / nx;
;             if (og + 1u == (tg + 1u) * nx) xb_add(&bar[XB_TOPGEN], 1u);
;             else XB_SPIN(xb_ld(&bar[XB_TOPGEN]) == tg, bar);
;             __builtin_amdgcn_fence(__ATOMIC_ACQUIRE, "agent");
;             xb_add(&bar[XB_XGEN(b.x)], 1u);
;             asm volatile("s_waitcnt vmcnt(0)" ::: "memory");
;         } else {
;             XB_SPIN(xb_ld(&bar[XB_XGEN(b.x)]) == gen, bar);
;             __builtin_amdgcn_fence(__ATOMIC_ACQUIRE, "agent");
;             asm volatile("s_waitcnt vmcnt(0)" ::: "memory");
;         }
;     }
;     __syncthreads();
; }
; __global__ void __launch_bounds__(NTHR, 2) fwd(Args args) {
;     ...
;     SEAM(1);
.LBB0_129:
	v_readlane_b32 s4, v255, 11
	v_readlane_b32 s5, v255, 12
	s_cmp_gt_i32 s5, 2
	s_cselect_b64 s[6:7], -1, 0
	s_and_b64 s[0:1], s[0:1], s[6:7]
	s_andn2_b64 vcc, exec, s[0:1]
	s_cbranch_vccnz .LBB0_183
	s_waitcnt vmcnt(0)
	s_waitcnt lgkmcnt(0)
	s_barrier
	s_mov_b64 s[0:1], exec
	v_readlane_b32 s4, v255, 7
	v_readlane_b32 s5, v255, 8
	s_and_b64 s[4:5], s[0:1], s[4:5]
	s_mov_b64 exec, s[4:5]
	s_cbranch_execz .LBB0_182
	s_add_i32 s3, 0, 0x20160
	v_mov_b32_e32 v1, s3
	ds_read_b64 v[2:3], v1
	v_readlane_b32 s8, v255, 6
	s_lshl_b32 s9, s8, 8
	s_add_u32 s10, s9, 0x5400
	v_mov_b32_e32 v4, s10
	v_mov_b32_e32 v5, 1
	s_waitcnt lgkmcnt(0)
	v_readfirstlane_b32 s12, v2
	v_readfirstlane_b32 s13, v3
	global_atomic_add v6, v4, v5, s[50:51] sc0
	s_add_u32 s14, s101, 1
	s_mul_i32 s15, s14, s12
	s_mul_i32 s16, s14, s13
	s_add_u32 s17, s9, 0x6400
	v_mov_b32_e32 v7, s17
	s_waitcnt vmcnt(0)
	v_readfirstlane_b32 s18, v6
	s_add_u32 s18, s18, 1
	s_cmp_lg_u32 s18, s15
	s_cbranch_scc1 .Lgb1_wait
	buffer_wbl2 sc1
	s_waitcnt vmcnt(0)
	v_mov_b32_e32 v8, 0x7400
	global_atomic_add v9, v8, v5, s[50:51] sc0
	s_waitcnt vmcnt(0)
	v_readfirstlane_b32 s19, v9
	s_add_u32 s19, s19, 1
	s_cmp_lg_u32 s19, s16
	s_cbranch_scc1 .Lgb1_wait
	v_mov_b32_e32 v8, 0x6400
	global_atomic_add v8, v5, s[50:51]
	global_atomic_add v8, v5, s[50:51] offset:256
	global_atomic_add v8, v5, s[50:51] offset:512
	global_atomic_add v8, v5, s[50:51] offset:768
	global_atomic_add v8, v5, s[50:51] offset:1024
	global_atomic_add v8, v5, s[50:51] offset:1280
	global_atomic_add v8, v5, s[50:51] offset:1536
	global_atomic_add v8, v5, s[50:51] offset:1792
	global_atomic_add v8, v5, s[50:51] offset:2048
	global_atomic_add v8, v5, s[50:51] offset:2304
	global_atomic_add v8, v5, s[50:51] offset:2560
	global_atomic_add v8, v5, s[50:51] offset:2816
	global_atomic_add v8, v5, s[50:51] offset:3072
	global_atomic_add v8, v5, s[50:51] offset:3328
	global_atomic_add v8, v5, s[50:51] offset:3584
	global_atomic_add v8, v5, s[50:51] offset:3840
	v_mov_b32_e32 v8, 0x7500
	global_atomic_add v8, v5, s[50:51]
	s_branch .Lgb1_acq
.Lgb1_wait:
	s_mov_b32 s20, 0
.Lgb1_spin:
	global_load_dword v10, v7, s[50:51] sc1
	s_waitcnt vmcnt(0)
	v_readfirstlane_b32 s21, v10
	s_cmp_lg_u32 s21, s101
	s_cbranch_scc1 .Lgb1_acq
	s_sleep 1
	s_add_u32 s20, s20, 1
	s_cmp_lt_u32 s20, 0x100000
	s_cbranch_scc1 .Lgb1_spin
.Lgb1_acq:
	s_waitcnt vmcnt(0)
	buffer_inv sc1
	s_waitcnt vmcnt(0)
	s_add_u32 s101, s101, 1

; __device__ __forceinline__ unsigned xb_ld(unsigned* p)              { return __hip_atomic_load(p, __ATOMIC_RELAXED, __HIP_MEMORY_SCOPE_AGENT); }
; __device__ __forceinline__ unsigned xb_add(unsigned* p, unsigned v) { return __hip_atomic_fetch_add(p, v, __ATOMIC_RELAXED, __HIP_MEMORY_SCOPE_AGENT); }
; #define XB_SPIN(cond, bar) do { unsigned _sp = 0; while (cond) { __builtin_amdgcn_s_sleep(1); \
;     if ((++_sp & 255u) == 0u) { if (xb_ld(&(bar)[XB_TMO])) break; if (_sp > XB_SPIN_CAP) { atomicAdd(&(bar)[XB_TMO], 1u); break; } } } } while (0)
; #define SEAM(k) do { if (IN(k) && IN((k) + 1)) GRID_BAR(); } while (0)
; __device__ __forceinline__ void xcd_barrier(const XcdBarrier& b) {
;     asm volatile("s_waitcnt vmcnt(0)" ::: "memory");
;     __syncthreads();
;     if (threadIdx.x == 0) {
;         unsigned* bar = b.bar;
;         __builtin_amdgcn_s_waitcnt(0);
;         unsigned nloc = b.st[0], nx = b.st[1];
;         if (nloc == 0u) { xcd_barrier_complete(bar, b.x, nloc, nx); b.st[0] = nloc; b.st[1] = nx; }
;         const unsigned old = xb_add(&bar[XB_XSUB(b.x)], 1u);
;         const unsigned gen = old / nloc;
;         if (old + 1u == (gen + 1u) * nloc) {
;             __builtin_amdgcn_fence(__ATOMIC_RELEASE, "agent");
;             asm volatile("s_waitcnt vmcnt(0)" ::: "memory");
;             const unsigned og = xb_add(&bar[XB_TOP], 1u);
;             const unsigned tg = og / nx;
;             if (og + 1u == (tg + 1u) * nx) xb_add(&bar[XB_TOPGEN], 1u);
;             else XB_SPIN(xb_ld(&bar[XB_TOPGEN]) == tg, bar);
;             __builtin_amdgcn_fence(__ATOMIC_ACQUIRE, "agent");
;             xb_add(&bar[XB_XGEN(b.x)], 1u);
;             asm volatile("s_waitcnt vmcnt(0)" ::: "memory");
;         } else {
;             XB_SPIN(xb_ld(&bar[XB_XGEN(b.x)]) == gen, bar);
;             __builtin_amdgcn_fence(__ATOMIC_ACQUIRE, "agent");
;             asm volatile("s_waitcnt vmcnt(0)" ::: "memory");
;         }
;     }
;     __syncthreads();
; }
; template <int L>
; __device__ __forceinline__ void layer(Frame& F, const XcdBarrier& bar, float* out, const int lo, const int hi) {
;     ...
;     SEAM(pb + 0);
.LBB0_224:
	v_readlane_b32 s0, v255, 11
	v_readlane_b32 s1, v255, 12
	s_cmp_gt_i32 s1, 3
	s_cselect_b64 s[6:7], -1, 0
	s_and_b64 s[0:1], s[10:11], s[6:7]
	s_andn2_b64 vcc, exec, s[0:1]
	s_cbranch_vccnz .LBB0_278
	s_waitcnt vmcnt(0)
	s_waitcnt lgkmcnt(0)
	s_barrier
	s_mov_b64 s[0:1], exec
	v_readlane_b32 s4, v255, 7
	v_readlane_b32 s5, v255, 8
	s_and_b64 s[4:5], s[0:1], s[4:5]
	s_mov_b64 exec, s[4:5]
	s_cbranch_execz .LBB0_277
	s_add_i32 s3, 0, 0x20160
	v_mov_b32_e32 v1, s3
	ds_read_b64 v[2:3], v1
	v_readlane_b32 s8, v255, 6
	s_lshl_b32 s9, s8, 8
	s_add_u32 s10, s9, 0x5400
	v_mov_b32_e32 v4, s10
	v_mov_b32_e32 v5, 1
	s_waitcnt lgkmcnt(0)
	v_readfirstlane_b32 s12, v2
	v_readfirstlane_b32 s13, v3
	global_atomic_add v6, v4, v5, s[50:51] sc0
	s_add_u32 s14, s101, 1
	s_mul_i32 s15, s14, s12
	s_mul_i32 s16, s14, s13
	s_add_u32 s17, s9, 0x6400
	v_mov_b32_e32 v7, s17
	s_waitcnt vmcnt(0)
	v_readfirstlane_b32 s18, v6
	s_add_u32 s18, s18, 1
	s_cmp_lg_u32 s18, s15
	s_cbranch_scc1 .Lgb2_wait
	buffer_wbl2 sc1
	s_waitcnt vmcnt(0)
	v_mov_b32_e32 v8, 0x7400
	global_atomic_add v9, v8, v5, s[50:51] sc0
	s_waitcnt vmcnt(0)
	v_readfirstlane_b32 s19, v9
	s_add_u32 s19, s19, 1
	s_cmp_lg_u32 s19, s16
	s_cbranch_scc1 .Lgb2_wait
	v_mov_b32_e32 v8, 0x6400
	global_atomic_add v8, v5, s[50:51]
	global_atomic_add v8, v5, s[50:51] offset:256
	global_atomic_add v8, v5, s[50:51] offset:512
	global_atomic_add v8, v5, s[50:51] offset:768
	global_atomic_add v8, v5, s[50:51] offset:1024
	global_atomic_add v8, v5, s[50:51] offset:1280
	global_atomic_add v8, v5, s[50:51] offset:1536
	global_atomic_add v8, v5, s[50:51] offset:1792
	global_atomic_add v8, v5, s[50:51] offset:2048
	global_atomic_add v8, v5, s[50:51] offset:2304
	global_atomic_add v8, v5, s[50:51] offset:2560
	global_atomic_add v8, v5, s[50:51] offset:2816
	global_atomic_add v8, v5, s[50:51] offset:3072
	global_atomic_add v8, v5, s[50:51] offset:3328
	global_atomic_add v8, v5, s[50:51] offset:3584
	global_atomic_add v8, v5, s[50:51] offset:3840
	v_mov_b32_e32 v8, 0x7500
	global_atomic_add v8, v5, s[50:51]
	s_branch .Lgb2_acq

; __device__ __forceinline__ unsigned xb_ld(unsigned* p)              { return __hip_atomic_load(p, __ATOMIC_RELAXED, __HIP_MEMORY_SCOPE_AGENT); }
; __device__ __forceinline__ unsigned xb_add(unsigned* p, unsigned v) { return __hip_atomic_fetch_add(p, v, __ATOMIC_RELAXED, __HIP_MEMORY_SCOPE_AGENT); }
; #define XB_SPIN(cond, bar) do { unsigned _sp = 0; while (cond) { __builtin_amdgcn_s_sleep(1); \
;     if ((++_sp & 255u) == 0u) { if (xb_ld(&(bar)[XB_TMO])) break; if (_sp > XB_SPIN_CAP) { atomicAdd(&(bar)[XB_TMO], 1u); break; } } } } while (0)
; #define SEAM(k) do { if (IN(k) && IN((k) + 1)) GRID_BAR(); } while (0)
; __device__ __forceinline__ void xcd_barrier(const XcdBarrier& b) {
;     asm volatile("s_waitcnt vmcnt(0)" ::: "memory");
;     __syncthreads();
;     if (threadIdx.x == 0) {
;         unsigned* bar = b.bar;
;         __builtin_amdgcn_s_waitcnt(0);
;         unsigned nloc = b.st[0], nx = b.st[1];
;         if (nloc == 0u) { xcd_barrier_complete(bar, b.x, nloc, nx); b.st[0] = nloc; b.st[1] = nx; }
;         const unsigned old = xb_add(&bar[XB_XSUB(b.x)], 1u);
;         const unsigned gen = old / nloc;
;         if (old + 1u == (gen + 1u) * nloc) {
;             __builtin_amdgcn_fence(__ATOMIC_RELEASE, "agent");
;             asm volatile("s_waitcnt vmcnt(0)" ::: "memory");
;             const unsigned og = xb_add(&bar[XB_TOP], 1u);
;             const unsigned tg = og / nx;
;             if (og + 1u == (tg + 1u) * nx) xb_add(&bar[XB_TOPGEN], 1u);
;             else XB_SPIN(xb_ld(&bar[XB_TOPGEN]) == tg, bar);
;             __builtin_amdgcn_fence(__ATOMIC_ACQUIRE, "agent");
;             xb_add(&bar[XB_XGEN(b.x)], 1u);
;             asm volatile("s_waitcnt vmcnt(0)" ::: "memory");
;         } else {
;             XB_SPIN(xb_ld(&bar[XB_XGEN(b.x)]) == gen, bar);
;             __builtin_amdgcn_fence(__ATOMIC_ACQUIRE, "agent");
;             asm volatile("s_waitcnt vmcnt(0)" ::: "memory");
;         }
;     }
;     __syncthreads();
; }
; template <int L>
; __device__ __forceinline__ void layer(Frame& F, const XcdBarrier& bar, float* out, const int lo, const int hi) {
;     ...
;     SEAM(pb + 1);
.LBB0_303:
	v_readlane_b32 s4, v255, 11
	v_readlane_b32 s5, v255, 12
	s_cmp_gt_i32 s5, 4
	s_cselect_b64 s[6:7], -1, 0
	s_and_b64 s[0:1], s[0:1], s[6:7]
	s_andn2_b64 vcc, exec, s[0:1]
	s_cbranch_vccnz .LBB0_357
	s_waitcnt vmcnt(0)
	s_waitcnt lgkmcnt(0)
	s_barrier
	s_mov_b64 s[0:1], exec
	v_readlane_b32 s4, v255, 7
	v_readlane_b32 s5, v255, 8
	s_and_b64 s[4:5], s[0:1], s[4:5]
	s_mov_b64 exec, s[4:5]
	s_cbranch_execz .LBB0_356
	s_add_i32 s3, 0, 0x20160
	v_mov_b32_e32 v1, s3
	ds_read_b64 v[2:3], v1
	v_readlane_b32 s8, v255, 6
	s_lshl_b32 s9, s8, 8
	s_add_u32 s10, s9, 0x5400
	v_mov_b32_e32 v4, s10
	v_mov_b32_e32 v5, 1
	s_waitcnt lgkmcnt(0)
	v_readfirstlane_b32 s12, v2
	v_readfirstlane_b32 s13, v3
	global_atomic_add v6, v4, v5, s[50:51] sc0
	s_add_u32 s14, s101, 1
	s_mul_i32 s15, s14, s12
	s_mul_i32 s16, s14, s13
	s_add_u32 s17, s9, 0x6400
	v_mov_b32_e32 v7, s17
	s_waitcnt vmcnt(0)
	v_readfirstlane_b32 s18, v6
	s_add_u32 s18, s18, 1
	s_cmp_lg_u32 s18, s15
	s_cbranch_scc1 .Lgb3_wait
	buffer_wbl2 sc1
	s_waitcnt vmcnt(0)
	v_mov_b32_e32 v8, 0x7400
	global_atomic_add v9, v8, v5, s[50:51] sc0
	s_waitcnt vmcnt(0)
	v_readfirstlane_b32 s19, v9
	s_add_u32 s19, s19, 1
	s_cmp_lg_u32 s19, s16
	s_cbranch_scc1 .Lgb3_wait
	v_mov_b32_e32 v8, 0x6400
	global_atomic_add v8, v5, s[50:51]
	global_atomic_add v8, v5, s[50:51] offset:256
	global_atomic_add v8, v5, s[50:51] offset:512
	global_atomic_add v8, v5, s[50:51] offset:768
	global_atomic_add v8, v5, s[50:51] offset:1024
	global_atomic_add v8, v5, s[50:51] offset:1280
	global_atomic_add v8, v5, s[50:51] offset:1536
	global_atomic_add v8, v5, s[50:51] offset:1792
	global_atomic_add v8, v5, s[50:51] offset:2048
	global_atomic_add v8, v5, s[50:51] offset:2304
	global_atomic_add v8, v5, s[50:51] offset:2560
	global_atomic_add v8, v5, s[50:51] offset:2816
	global_atomic_add v8, v5, s[50:51] offset:3072
	global_atomic_add v8, v5, s[50:51] offset:3328
	global_atomic_add v8, v5, s[50:51] offset:3584
	global_atomic_add v8, v5, s[50:51] offset:3840
	v_mov_b32_e32 v8, 0x7500
	global_atomic_add v8, v5, s[50:51]
	s_branch .Lgb3_acq

; __device__ __forceinline__ unsigned xb_ld(unsigned* p)              { return __hip_atomic_load(p, __ATOMIC_RELAXED, __HIP_MEMORY_SCOPE_AGENT); }
; __device__ __forceinline__ unsigned xb_add(unsigned* p, unsigned v) { return __hip_atomic_fetch_add(p, v, __ATOMIC_RELAXED, __HIP_MEMORY_SCOPE_AGENT); }
; #define XB_SPIN(cond, bar) do { unsigned _sp = 0; while (cond) { __builtin_amdgcn_s_sleep(1); \
;     if ((++_sp & 255u) == 0u) { if (xb_ld(&(bar)[XB_TMO])) break; if (_sp > XB_SPIN_CAP) { atomicAdd(&(bar)[XB_TMO], 1u); break; } } } } while (0)
; #define GRID_BAR() do { if (N_LAUNCHES == 1) xcd_barrier(bar); } while (0)
; __device__ __forceinline__ void xcd_barrier(const XcdBarrier& b) {
;     asm volatile("s_waitcnt vmcnt(0)" ::: "memory");
;     __syncthreads();
;     if (threadIdx.x == 0) {
;         unsigned* bar = b.bar;
;         __builtin_amdgcn_s_waitcnt(0);
;         unsigned nloc = b.st[0], nx = b.st[1];
;         if (nloc == 0u) { xcd_barrier_complete(bar, b.x, nloc, nx); b.st[0] = nloc; b.st[1] = nx; }
;         const unsigned old = xb_add(&bar[XB_XSUB(b.x)], 1u);
;         const unsigned gen = old / nloc;
;         if (old + 1u == (gen + 1u) * nloc) {
;             __builtin_amdgcn_fence(__ATOMIC_RELEASE, "agent");
;             asm volatile("s_waitcnt vmcnt(0)" ::: "memory");
;             const unsigned og = xb_add(&bar[XB_TOP], 1u);
;             const unsigned tg = og / nx;
;             if (og + 1u == (tg + 1u) * nx) xb_add(&bar[XB_TOPGEN], 1u);
;             else XB_SPIN(xb_ld(&bar[XB_TOPGEN]) == tg, bar);
;             __builtin_amdgcn_fence(__ATOMIC_ACQUIRE, "agent");
;             xb_add(&bar[XB_XGEN(b.x)], 1u);
;             asm volatile("s_waitcnt vmcnt(0)" ::: "memory");
;         } else {
;             XB_SPIN(xb_ld(&bar[XB_XGEN(b.x)]) == gen, bar);
;             __builtin_amdgcn_fence(__ATOMIC_ACQUIRE, "agent");
;             asm volatile("s_waitcnt vmcnt(0)" ::: "memory");
;         }
;     }
;     __syncthreads();
; }
; template <int L>
; __device__ __forceinline__ void layer(Frame& F, const XcdBarrier& bar, float* out, const int lo, const int hi) {
;     ...
;         GRID_BAR();
.LBB0_451:
	s_waitcnt vmcnt(0)
	s_waitcnt lgkmcnt(0)
	s_barrier
	s_mov_b64 s[0:1], exec
	v_readlane_b32 s6, v255, 7
	v_readlane_b32 s7, v255, 8
	s_and_b64 s[6:7], s[0:1], s[6:7]
	s_mov_b64 exec, s[6:7]
	s_cbranch_execz .LBB0_503
	s_add_i32 s3, 0, 0x20160
	v_mov_b32_e32 v1, s3
	ds_read_b64 v[2:3], v1
	v_readlane_b32 s8, v255, 6
	s_lshl_b32 s9, s8, 8
	s_add_u32 s10, s9, 0x5400
	v_mov_b32_e32 v4, s10
	v_mov_b32_e32 v5, 1
	s_waitcnt lgkmcnt(0)
	v_readfirstlane_b32 s12, v2
	v_readfirstlane_b32 s13, v3
	global_atomic_add v6, v4, v5, s[50:51] sc0
	s_add_u32 s14, s101, 1
	s_mul_i32 s15, s14, s12
	s_mul_i32 s16, s14, s13
	s_add_u32 s17, s9, 0x6400
	v_mov_b32_e32 v7, s17
	s_waitcnt vmcnt(0)
	v_readfirstlane_b32 s18, v6
	s_add_u32 s18, s18, 1
	s_cmp_lg_u32 s18, s15
	s_cbranch_scc1 .Lgb4_wait
	buffer_wbl2 sc1
	s_waitcnt vmcnt(0)
	v_mov_b32_e32 v8, 0x7400
	global_atomic_add v9, v8, v5, s[50:51] sc0
	s_waitcnt vmcnt(0)
	v_readfirstlane_b32 s19, v9
	s_add_u32 s19, s19, 1
	s_cmp_lg_u32 s19, s16
	s_cbranch_scc1 .Lgb4_wait
	v_mov_b32_e32 v8, 0x6400
	global_atomic_add v8, v5, s[50:51]
	global_atomic_add v8, v5, s[50:51] offset:256
	global_atomic_add v8, v5, s[50:51] offset:512
	global_atomic_add v8, v5, s[50:51] offset:768
	global_atomic_add v8, v5, s[50:51] offset:1024
	global_atomic_add v8, v5, s[50:51] offset:1280
	global_atomic_add v8, v5, s[50:51] offset:1536
	global_atomic_add v8, v5, s[50:51] offset:1792
	global_atomic_add v8, v5, s[50:51] offset:2048
	global_atomic_add v8, v5, s[50:51] offset:2304
	global_atomic_add v8, v5, s[50:51] offset:2560
	global_atomic_add v8, v5, s[50:51] offset:2816
	global_atomic_add v8, v5, s[50:51] offset:3072
	global_atomic_add v8, v5, s[50:51] offset:3328
	global_atomic_add v8, v5, s[50:51] offset:3584
	global_atomic_add v8, v5, s[50:51] offset:3840
	v_mov_b32_e32 v8, 0x7500
	global_atomic_add v8, v5, s[50:51]
	s_branch .Lgb4_acq

; __device__ __forceinline__ unsigned xb_ld(unsigned* p)              { return __hip_atomic_load(p, __ATOMIC_RELAXED, __HIP_MEMORY_SCOPE_AGENT); }
; __device__ __forceinline__ unsigned xb_add(unsigned* p, unsigned v) { return __hip_atomic_fetch_add(p, v, __ATOMIC_RELAXED, __HIP_MEMORY_SCOPE_AGENT); }
; #define XB_SPIN(cond, bar) do { unsigned _sp = 0; while (cond) { __builtin_amdgcn_s_sleep(1); \
;     if ((++_sp & 255u) == 0u) { if (xb_ld(&(bar)[XB_TMO])) break; if (_sp > XB_SPIN_CAP) { atomicAdd(&(bar)[XB_TMO], 1u); break; } } } } while (0)
; #define SEAM(k) do { if (IN(k) && IN((k) + 1)) GRID_BAR(); } while (0)
; __device__ __forceinline__ void xcd_barrier(const XcdBarrier& b) {
;     asm volatile("s_waitcnt vmcnt(0)" ::: "memory");
;     __syncthreads();
;     if (threadIdx.x == 0) {
;         unsigned* bar = b.bar;
;         __builtin_amdgcn_s_waitcnt(0);
;         unsigned nloc = b.st[0], nx = b.st[1];
;         if (nloc == 0u) { xcd_barrier_complete(bar, b.x, nloc, nx); b.st[0] = nloc; b.st[1] = nx; }
;         const unsigned old = xb_add(&bar[XB_XSUB(b.x)], 1u);
;         const unsigned gen = old / nloc;
;         if (old + 1u == (gen + 1u) * nloc) {
;             __builtin_amdgcn_fence(__ATOMIC_RELEASE, "agent");
;             asm volatile("s_waitcnt vmcnt(0)" ::: "memory");
;             const unsigned og = xb_add(&bar[XB_TOP], 1u);
;             const unsigned tg = og / nx;
;             if (og + 1u == (tg + 1u) * nx) xb_add(&bar[XB_TOPGEN], 1u);
;             else XB_SPIN(xb_ld(&bar[XB_TOPGEN]) == tg, bar);
;             __builtin_amdgcn_fence(__ATOMIC_ACQUIRE, "agent");
;             xb_add(&bar[XB_XGEN(b.x)], 1u);
;             asm volatile("s_waitcnt vmcnt(0)" ::: "memory");
;         } else {
;             XB_SPIN(xb_ld(&bar[XB_XGEN(b.x)]) == gen, bar);
;             __builtin_amdgcn_fence(__ATOMIC_ACQUIRE, "agent");
;             asm volatile("s_waitcnt vmcnt(0)" ::: "memory");
;         }
;     }
;     __syncthreads();
; }
; template <int L>
; __device__ __forceinline__ void layer(Frame& F, const XcdBarrier& bar, float* out, const int lo, const int hi) {
;     ...
;     SEAM(pb + 2);
.LBB0_946:
	v_readlane_b32 s0, v255, 11
	v_readlane_b32 s1, v255, 12
	s_cmp_gt_i32 s1, 5
	v_readlane_b32 s0, v255, 30
	s_cselect_b64 s[6:7], -1, 0
	v_readlane_b32 s1, v255, 31
	s_and_b64 s[0:1], s[0:1], s[6:7]
	s_andn2_b64 vcc, exec, s[0:1]
	s_cbranch_vccnz .LBB0_1000
	s_waitcnt vmcnt(0)
	s_waitcnt lgkmcnt(0)
	s_barrier
	s_mov_b64 s[0:1], exec
	v_readlane_b32 s8, v255, 7
	v_readlane_b32 s9, v255, 8
	s_and_b64 s[8:9], s[0:1], s[8:9]
	s_mov_b64 exec, s[8:9]
	s_cbranch_execz .LBB0_999
	s_add_i32 s3, 0, 0x20160
	v_mov_b32_e32 v1, s3
	ds_read_b64 v[2:3], v1
	v_readlane_b32 s8, v255, 6
	s_lshl_b32 s9, s8, 8
	s_add_u32 s10, s9, 0x5400
	v_mov_b32_e32 v4, s10
	v_mov_b32_e32 v5, 1
	s_waitcnt lgkmcnt(0)
	v_readfirstlane_b32 s12, v2
	v_readfirstlane_b32 s13, v3
	global_atomic_add v6, v4, v5, s[50:51] sc0
	s_add_u32 s14, s101, 1
	s_mul_i32 s15, s14, s12
	s_mul_i32 s16, s14, s13
	s_add_u32 s17, s9, 0x6400
	v_mov_b32_e32 v7, s17
	s_waitcnt vmcnt(0)
	v_readfirstlane_b32 s18, v6
	s_add_u32 s18, s18, 1
	s_cmp_lg_u32 s18, s15
	s_cbranch_scc1 .Lgb5_wait
	buffer_wbl2 sc1
	s_waitcnt vmcnt(0)
	v_mov_b32_e32 v8, 0x7400
	global_atomic_add v9, v8, v5, s[50:51] sc0
	s_waitcnt vmcnt(0)
	v_readfirstlane_b32 s19, v9
	s_add_u32 s19, s19, 1
	s_cmp_lg_u32 s19, s16
	s_cbranch_scc1 .Lgb5_wait
	v_mov_b32_e32 v8, 0x6400
	global_atomic_add v8, v5, s[50:51]
	global_atomic_add v8, v5, s[50:51] offset:256
	global_atomic_add v8, v5, s[50:51] offset:512
	global_atomic_add v8, v5, s[50:51] offset:768
	global_atomic_add v8, v5, s[50:51] offset:1024
	global_atomic_add v8, v5, s[50:51] offset:1280
	global_atomic_add v8, v5, s[50:51] offset:1536
	global_atomic_add v8, v5, s[50:51] offset:1792
	global_atomic_add v8, v5, s[50:51] offset:2048
	global_atomic_add v8, v5, s[50:51] offset:2304
	global_atomic_add v8, v5, s[50:51] offset:2560
	global_atomic_add v8, v5, s[50:51] offset:2816
	global_atomic_add v8, v5, s[50:51] offset:3072
	global_atomic_add v8, v5, s[50:51] offset:3328
	global_atomic_add v8, v5, s[50:51] offset:3584
	global_atomic_add v8, v5, s[50:51] offset:3840
	v_mov_b32_e32 v8, 0x7500
	global_atomic_add v8, v5, s[50:51]
	s_branch .Lgb5_acq

; __device__ __forceinline__ unsigned xb_ld(unsigned* p)              { return __hip_atomic_load(p, __ATOMIC_RELAXED, __HIP_MEMORY_SCOPE_AGENT); }
; __device__ __forceinline__ unsigned xb_add(unsigned* p, unsigned v) { return __hip_atomic_fetch_add(p, v, __ATOMIC_RELAXED, __HIP_MEMORY_SCOPE_AGENT); }
; #define XB_SPIN(cond, bar) do { unsigned _sp = 0; while (cond) { __builtin_amdgcn_s_sleep(1); \
;     if ((++_sp & 255u) == 0u) { if (xb_ld(&(bar)[XB_TMO])) break; if (_sp > XB_SPIN_CAP) { atomicAdd(&(bar)[XB_TMO], 1u); break; } } } } while (0)
; #define SEAM(k) do { if (IN(k) && IN((k) + 1)) GRID_BAR(); } while (0)
; __device__ __forceinline__ void xcd_barrier(const XcdBarrier& b) {
;     asm volatile("s_waitcnt vmcnt(0)" ::: "memory");
;     __syncthreads();
;     if (threadIdx.x == 0) {
;         unsigned* bar = b.bar;
;         __builtin_amdgcn_s_waitcnt(0);
;         unsigned nloc = b.st[0], nx = b.st[1];
;         if (nloc == 0u) { xcd_barrier_complete(bar, b.x, nloc, nx); b.st[0] = nloc; b.st[1] = nx; }
;         const unsigned old = xb_add(&bar[XB_XSUB(b.x)], 1u);
;         const unsigned gen = old / nloc;
;         if (old + 1u == (gen + 1u) * nloc) {
;             __builtin_amdgcn_fence(__ATOMIC_RELEASE, "agent");
;             asm volatile("s_waitcnt vmcnt(0)" ::: "memory");
;             const unsigned og = xb_add(&bar[XB_TOP], 1u);
;             const unsigned tg = og / nx;
;             if (og + 1u == (tg + 1u) * nx) xb_add(&bar[XB_TOPGEN], 1u);
;             else XB_SPIN(xb_ld(&bar[XB_TOPGEN]) == tg, bar);
;             __builtin_amdgcn_fence(__ATOMIC_ACQUIRE, "agent");
;             xb_add(&bar[XB_XGEN(b.x)], 1u);
;             asm volatile("s_waitcnt vmcnt(0)" ::: "memory");
;         } else {
;             XB_SPIN(xb_ld(&bar[XB_XGEN(b.x)]) == gen, bar);
;             __builtin_amdgcn_fence(__ATOMIC_ACQUIRE, "agent");
;             asm volatile("s_waitcnt vmcnt(0)" ::: "memory");
;         }
;     }
;     __syncthreads();
; }
; template <int L>
; __device__ __forceinline__ void layer(Frame& F, const XcdBarrier& bar, float* out, const int lo, const int hi) {
;     ...
;     SEAM(pb + 3);
.LBB0_1025:
	v_readlane_b32 s6, v255, 11
	v_readlane_b32 s7, v255, 12
	s_cmp_gt_i32 s7, 6
	s_cselect_b64 s[6:7], -1, 0
	s_and_b64 s[0:1], s[0:1], s[6:7]
	s_andn2_b64 vcc, exec, s[0:1]
	s_cbranch_vccnz .LBB0_1079
	s_waitcnt vmcnt(0)
	s_waitcnt vmcnt(0) lgkmcnt(0)
	s_barrier
	s_mov_b64 s[0:1], exec
	v_readlane_b32 s8, v255, 7
	v_readlane_b32 s9, v255, 8
	s_and_b64 s[8:9], s[0:1], s[8:9]
	s_mov_b64 exec, s[8:9]
	s_cbranch_execz .LBB0_1078
	s_add_i32 s3, 0, 0x20160
	v_mov_b32_e32 v1, s3
	ds_read_b64 v[2:3], v1
	v_readlane_b32 s8, v255, 6
	s_lshl_b32 s9, s8, 8
	s_add_u32 s10, s9, 0x5400
	v_mov_b32_e32 v4, s10
	v_mov_b32_e32 v5, 1
	s_waitcnt lgkmcnt(0)
	v_readfirstlane_b32 s12, v2
	v_readfirstlane_b32 s13, v3
	global_atomic_add v6, v4, v5, s[50:51] sc0
	s_add_u32 s14, s101, 1
	s_mul_i32 s15, s14, s12
	s_mul_i32 s16, s14, s13
	s_add_u32 s17, s9, 0x6400
	v_mov_b32_e32 v7, s17
	s_waitcnt vmcnt(0)
	v_readfirstlane_b32 s18, v6
	s_add_u32 s18, s18, 1
	s_cmp_lg_u32 s18, s15
	s_cbranch_scc1 .Lgb6_wait
	buffer_wbl2 sc1
	s_waitcnt vmcnt(0)
	v_mov_b32_e32 v8, 0x7400
	global_atomic_add v9, v8, v5, s[50:51] sc0
	s_waitcnt vmcnt(0)
	v_readfirstlane_b32 s19, v9
	s_add_u32 s19, s19, 1
	s_cmp_lg_u32 s19, s16
	s_cbranch_scc1 .Lgb6_wait
	v_mov_b32_e32 v8, 0x6400
	global_atomic_add v8, v5, s[50:51]
	global_atomic_add v8, v5, s[50:51] offset:256
	global_atomic_add v8, v5, s[50:51] offset:512
	global_atomic_add v8, v5, s[50:51] offset:768
	global_atomic_add v8, v5, s[50:51] offset:1024
	global_atomic_add v8, v5, s[50:51] offset:1280
	global_atomic_add v8, v5, s[50:51] offset:1536
	global_atomic_add v8, v5, s[50:51] offset:1792
	global_atomic_add v8, v5, s[50:51] offset:2048
	global_atomic_add v8, v5, s[50:51] offset:2304
	global_atomic_add v8, v5, s[50:51] offset:2560
	global_atomic_add v8, v5, s[50:51] offset:2816
	global_atomic_add v8, v5, s[50:51] offset:3072
	global_atomic_add v8, v5, s[50:51] offset:3328
	global_atomic_add v8, v5, s[50:51] offset:3584
	global_atomic_add v8, v5, s[50:51] offset:3840
	v_mov_b32_e32 v8, 0x7500
	global_atomic_add v8, v5, s[50:51]
	s_branch .Lgb6_acq

; __device__ __forceinline__ unsigned xb_ld(unsigned* p)              { return __hip_atomic_load(p, __ATOMIC_RELAXED, __HIP_MEMORY_SCOPE_AGENT); }
; __device__ __forceinline__ unsigned xb_add(unsigned* p, unsigned v) { return __hip_atomic_fetch_add(p, v, __ATOMIC_RELAXED, __HIP_MEMORY_SCOPE_AGENT); }
; #define XB_SPIN(cond, bar) do { unsigned _sp = 0; while (cond) { __builtin_amdgcn_s_sleep(1); \
;     if ((++_sp & 255u) == 0u) { if (xb_ld(&(bar)[XB_TMO])) break; if (_sp > XB_SPIN_CAP) { atomicAdd(&(bar)[XB_TMO], 1u); break; } } } } while (0)
; #define SEAM(k) do { if (IN(k) && IN((k) + 1)) GRID_BAR(); } while (0)
; __device__ __forceinline__ void xcd_barrier(const XcdBarrier& b) {
;     asm volatile("s_waitcnt vmcnt(0)" ::: "memory");
;     __syncthreads();
;     if (threadIdx.x == 0) {
;         unsigned* bar = b.bar;
;         __builtin_amdgcn_s_waitcnt(0);
;         unsigned nloc = b.st[0], nx = b.st[1];
;         if (nloc == 0u) { xcd_barrier_complete(bar, b.x, nloc, nx); b.st[0] = nloc; b.st[1] = nx; }
;         const unsigned old = xb_add(&bar[XB_XSUB(b.x)], 1u);
;         const unsigned gen = old / nloc;
;         if (old + 1u == (gen + 1u) * nloc) {
;             __builtin_amdgcn_fence(__ATOMIC_RELEASE, "agent");
;             asm volatile("s_waitcnt vmcnt(0)" ::: "memory");
;             const unsigned og = xb_add(&bar[XB_TOP], 1u);
;             const unsigned tg = og / nx;
;             if (og + 1u == (tg + 1u) * nx) xb_add(&bar[XB_TOPGEN], 1u);
;             else XB_SPIN(xb_ld(&bar[XB_TOPGEN]) == tg, bar);
;             __builtin_amdgcn_fence(__ATOMIC_ACQUIRE, "agent");
;             xb_add(&bar[XB_XGEN(b.x)], 1u);
;             asm volatile("s_waitcnt vmcnt(0)" ::: "memory");
;         } else {
;             XB_SPIN(xb_ld(&bar[XB_XGEN(b.x)]) == gen, bar);
;             __builtin_amdgcn_fence(__ATOMIC_ACQUIRE, "agent");
;             asm volatile("s_waitcnt vmcnt(0)" ::: "memory");
;         }
;     }
;     __syncthreads();
; }
; template <int L>
; __device__ __forceinline__ void layer(Frame& F, const XcdBarrier& bar, float* out, const int lo, const int hi) {
;     ...
;     SEAM(pb + 4);
.LBB0_1090:
	v_readlane_b32 s6, v255, 11
	v_readlane_b32 s7, v255, 12
	s_cmp_gt_i32 s7, 7
	s_cselect_b64 s[6:7], -1, 0
	s_and_b64 s[0:1], s[0:1], s[6:7]
	s_andn2_b64 vcc, exec, s[0:1]
	s_cbranch_vccnz .LBB0_1144
	s_waitcnt vmcnt(0)
	s_waitcnt vmcnt(0) lgkmcnt(0)
	s_barrier
	s_mov_b64 s[0:1], exec
	v_readlane_b32 s8, v255, 7
	v_readlane_b32 s9, v255, 8
	s_and_b64 s[8:9], s[0:1], s[8:9]
	s_mov_b64 exec, s[8:9]
	s_cbranch_execz .LBB0_1143
	s_add_i32 s3, 0, 0x20160
	v_mov_b32_e32 v1, s3
	ds_read_b64 v[2:3], v1
	v_readlane_b32 s8, v255, 6
	s_lshl_b32 s9, s8, 8
	s_add_u32 s10, s9, 0x5400
	v_mov_b32_e32 v4, s10
	v_mov_b32_e32 v5, 1
	s_waitcnt lgkmcnt(0)
	v_readfirstlane_b32 s12, v2
	v_readfirstlane_b32 s13, v3
	global_atomic_add v6, v4, v5, s[50:51] sc0
	s_add_u32 s14, s101, 1
	s_mul_i32 s15, s14, s12
	s_mul_i32 s16, s14, s13
	s_add_u32 s17, s9, 0x6400
	v_mov_b32_e32 v7, s17
	s_waitcnt vmcnt(0)
	v_readfirstlane_b32 s18, v6
	s_add_u32 s18, s18, 1
	s_cmp_lg_u32 s18, s15
	s_cbranch_scc1 .Lgb7_wait
	buffer_wbl2 sc1
	s_waitcnt vmcnt(0)
	v_mov_b32_e32 v8, 0x7400
	global_atomic_add v9, v8, v5, s[50:51] sc0
	s_waitcnt vmcnt(0)
	v_readfirstlane_b32 s19, v9
	s_add_u32 s19, s19, 1
	s_cmp_lg_u32 s19, s16
	s_cbranch_scc1 .Lgb7_wait
	v_mov_b32_e32 v8, 0x6400
	global_atomic_add v8, v5, s[50:51]
	global_atomic_add v8, v5, s[50:51] offset:256
	global_atomic_add v8, v5, s[50:51] offset:512
	global_atomic_add v8, v5, s[50:51] offset:768
	global_atomic_add v8, v5, s[50:51] offset:1024
	global_atomic_add v8, v5, s[50:51] offset:1280
	global_atomic_add v8, v5, s[50:51] offset:1536
	global_atomic_add v8, v5, s[50:51] offset:1792
	global_atomic_add v8, v5, s[50:51] offset:2048
	global_atomic_add v8, v5, s[50:51] offset:2304
	global_atomic_add v8, v5, s[50:51] offset:2560
	global_atomic_add v8, v5, s[50:51] offset:2816
	global_atomic_add v8, v5, s[50:51] offset:3072
	global_atomic_add v8, v5, s[50:51] offset:3328
	global_atomic_add v8, v5, s[50:51] offset:3584
	global_atomic_add v8, v5, s[50:51] offset:3840
	v_mov_b32_e32 v8, 0x7500
	global_atomic_add v8, v5, s[50:51]
	s_branch .Lgb7_acq

; __device__ __forceinline__ unsigned xb_ld(unsigned* p)              { return __hip_atomic_load(p, __ATOMIC_RELAXED, __HIP_MEMORY_SCOPE_AGENT); }
; __device__ __forceinline__ unsigned xb_add(unsigned* p, unsigned v) { return __hip_atomic_fetch_add(p, v, __ATOMIC_RELAXED, __HIP_MEMORY_SCOPE_AGENT); }
; #define XB_SPIN(cond, bar) do { unsigned _sp = 0; while (cond) { __builtin_amdgcn_s_sleep(1); \
;     if ((++_sp & 255u) == 0u) { if (xb_ld(&(bar)[XB_TMO])) break; if (_sp > XB_SPIN_CAP) { atomicAdd(&(bar)[XB_TMO], 1u); break; } } } } while (0)
; #define SEAM(k) do { if (IN(k) && IN((k) + 1)) GRID_BAR(); } while (0)
; __device__ __forceinline__ void xcd_barrier(const XcdBarrier& b) {
;     asm volatile("s_waitcnt vmcnt(0)" ::: "memory");
;     __syncthreads();
;     if (threadIdx.x == 0) {
;         unsigned* bar = b.bar;
;         __builtin_amdgcn_s_waitcnt(0);
;         unsigned nloc = b.st[0], nx = b.st[1];
;         if (nloc == 0u) { xcd_barrier_complete(bar, b.x, nloc, nx); b.st[0] = nloc; b.st[1] = nx; }
;         const unsigned old = xb_add(&bar[XB_XSUB(b.x)], 1u);
;         const unsigned gen = old / nloc;
;         if (old + 1u == (gen + 1u) * nloc) {
;             __builtin_amdgcn_fence(__ATOMIC_RELEASE, "agent");
;             asm volatile("s_waitcnt vmcnt(0)" ::: "memory");
;             const unsigned og = xb_add(&bar[XB_TOP], 1u);
;             const unsigned tg = og / nx;
;             if (og + 1u == (tg + 1u) * nx) xb_add(&bar[XB_TOPGEN], 1u);
;             else XB_SPIN(xb_ld(&bar[XB_TOPGEN]) == tg, bar);
;             __builtin_amdgcn_fence(__ATOMIC_ACQUIRE, "agent");
;             xb_add(&bar[XB_XGEN(b.x)], 1u);
;             asm volatile("s_waitcnt vmcnt(0)" ::: "memory");
;         } else {
;             XB_SPIN(xb_ld(&bar[XB_XGEN(b.x)]) == gen, bar);
;             __builtin_amdgcn_fence(__ATOMIC_ACQUIRE, "agent");
;             asm volatile("s_waitcnt vmcnt(0)" ::: "memory");
;         }
;     }
;     __syncthreads();
; }
; template <int L>
; __device__ __forceinline__ void layer(Frame& F, const XcdBarrier& bar, float* out, const int lo, const int hi) {
;     ...
;         SEAM(pb + 5);
.LBB0_1161:
	v_readlane_b32 s6, v255, 11
	v_readlane_b32 s7, v255, 12
	s_cmp_gt_i32 s7, 8
	s_cselect_b64 s[6:7], -1, 0
	s_and_b64 s[0:1], s[0:1], s[6:7]
	s_andn2_b64 vcc, exec, s[0:1]
	s_cbranch_vccnz .LBB0_1215
	s_waitcnt vmcnt(0)
	s_waitcnt vmcnt(0) lgkmcnt(0)
	s_barrier
	s_mov_b64 s[0:1], exec
	v_readlane_b32 s8, v255, 7
	v_readlane_b32 s9, v255, 8
	s_and_b64 s[8:9], s[0:1], s[8:9]
	s_mov_b64 exec, s[8:9]
	s_cbranch_execz .LBB0_1214
	s_add_i32 s3, 0, 0x20160
	v_mov_b32_e32 v1, s3
	ds_read_b64 v[2:3], v1
	v_readlane_b32 s8, v255, 6
	s_lshl_b32 s9, s8, 8
	s_add_u32 s10, s9, 0x5400
	v_mov_b32_e32 v4, s10
	v_mov_b32_e32 v5, 1
	s_waitcnt lgkmcnt(0)
	v_readfirstlane_b32 s12, v2
	v_readfirstlane_b32 s13, v3
	global_atomic_add v6, v4, v5, s[50:51] sc0
	s_add_u32 s14, s101, 1
	s_mul_i32 s15, s14, s12
	s_mul_i32 s16, s14, s13
	s_add_u32 s17, s9, 0x6400
	v_mov_b32_e32 v7, s17
	s_waitcnt vmcnt(0)
	v_readfirstlane_b32 s18, v6
	s_add_u32 s18, s18, 1
	s_cmp_lg_u32 s18, s15
	s_cbranch_scc1 .Lgb8_wait
	buffer_wbl2 sc1
	s_waitcnt vmcnt(0)
	v_mov_b32_e32 v8, 0x7400
	global_atomic_add v9, v8, v5, s[50:51] sc0
	s_waitcnt vmcnt(0)
	v_readfirstlane_b32 s19, v9
	s_add_u32 s19, s19, 1
	s_cmp_lg_u32 s19, s16
	s_cbranch_scc1 .Lgb8_wait
	v_mov_b32_e32 v8, 0x6400
	global_atomic_add v8, v5, s[50:51]
	global_atomic_add v8, v5, s[50:51] offset:256
	global_atomic_add v8, v5, s[50:51] offset:512
	global_atomic_add v8, v5, s[50:51] offset:768
	global_atomic_add v8, v5, s[50:51] offset:1024
	global_atomic_add v8, v5, s[50:51] offset:1280
	global_atomic_add v8, v5, s[50:51] offset:1536
	global_atomic_add v8, v5, s[50:51] offset:1792
	global_atomic_add v8, v5, s[50:51] offset:2048
	global_atomic_add v8, v5, s[50:51] offset:2304
	global_atomic_add v8, v5, s[50:51] offset:2560
	global_atomic_add v8, v5, s[50:51] offset:2816
	global_atomic_add v8, v5, s[50:51] offset:3072
	global_atomic_add v8, v5, s[50:51] offset:3328
	global_atomic_add v8, v5, s[50:51] offset:3584
	global_atomic_add v8, v5, s[50:51] offset:3840
	v_mov_b32_e32 v8, 0x7500
	global_atomic_add v8, v5, s[50:51]
	s_branch .Lgb8_acq

; __device__ __forceinline__ unsigned xb_ld(unsigned* p)              { return __hip_atomic_load(p, __ATOMIC_RELAXED, __HIP_MEMORY_SCOPE_AGENT); }
; __device__ __forceinline__ unsigned xb_add(unsigned* p, unsigned v) { return __hip_atomic_fetch_add(p, v, __ATOMIC_RELAXED, __HIP_MEMORY_SCOPE_AGENT); }
; #define XB_SPIN(cond, bar) do { unsigned _sp = 0; while (cond) { __builtin_amdgcn_s_sleep(1); \
;     if ((++_sp & 255u) == 0u) { if (xb_ld(&(bar)[XB_TMO])) break; if (_sp > XB_SPIN_CAP) { atomicAdd(&(bar)[XB_TMO], 1u); break; } } } } while (0)
; #define SEAM(k) do { if (IN(k) && IN((k) + 1)) GRID_BAR(); } while (0)
; __device__ __forceinline__ void xcd_barrier(const XcdBarrier& b) {
;     asm volatile("s_waitcnt vmcnt(0)" ::: "memory");
;     __syncthreads();
;     if (threadIdx.x == 0) {
;         unsigned* bar = b.bar;
;         __builtin_amdgcn_s_waitcnt(0);
;         unsigned nloc = b.st[0], nx = b.st[1];
;         if (nloc == 0u) { xcd_barrier_complete(bar, b.x, nloc, nx); b.st[0] = nloc; b.st[1] = nx; }
;         const unsigned old = xb_add(&bar[XB_XSUB(b.x)], 1u);
;         const unsigned gen = old / nloc;
;         if (old + 1u == (gen + 1u) * nloc) {
;             __builtin_amdgcn_fence(__ATOMIC_RELEASE, "agent");
;             asm volatile("s_waitcnt vmcnt(0)" ::: "memory");
;             const unsigned og = xb_add(&bar[XB_TOP], 1u);
;             const unsigned tg = og / nx;
;             if (og + 1u == (tg + 1u) * nx) xb_add(&bar[XB_TOPGEN], 1u);
;             else XB_SPIN(xb_ld(&bar[XB_TOPGEN]) == tg, bar);
;             __builtin_amdgcn_fence(__ATOMIC_ACQUIRE, "agent");
;             xb_add(&bar[XB_XGEN(b.x)], 1u);
;             asm volatile("s_waitcnt vmcnt(0)" ::: "memory");
;         } else {
;             XB_SPIN(xb_ld(&bar[XB_XGEN(b.x)]) == gen, bar);
;             __builtin_amdgcn_fence(__ATOMIC_ACQUIRE, "agent");
;             asm volatile("s_waitcnt vmcnt(0)" ::: "memory");
;         }
;     }
;     __syncthreads();
; }
; template <int L>
; __device__ __forceinline__ void layer(Frame& F, const XcdBarrier& bar, float* out, const int lo, const int hi) {
;     ...
;         SEAM(pb + 6);
.LBB0_1244:
	v_readlane_b32 s6, v255, 11
	v_readlane_b32 s7, v255, 12
	s_cmp_gt_i32 s7, 9
	s_cselect_b64 s[6:7], -1, 0
	s_and_b64 s[0:1], s[0:1], s[6:7]
	s_andn2_b64 vcc, exec, s[0:1]
	s_cbranch_vccnz .LBB0_1298
	s_waitcnt vmcnt(0)
	s_waitcnt vmcnt(0) lgkmcnt(0)
	s_barrier
	s_mov_b64 s[0:1], exec
	v_readlane_b32 s8, v255, 7
	v_readlane_b32 s9, v255, 8
	s_and_b64 s[8:9], s[0:1], s[8:9]
	s_mov_b64 exec, s[8:9]
	s_cbranch_execz .LBB0_1297
	s_add_i32 s3, 0, 0x20160
	v_mov_b32_e32 v1, s3
	ds_read_b64 v[2:3], v1
	v_readlane_b32 s8, v255, 6
	s_lshl_b32 s9, s8, 8
	s_add_u32 s10, s9, 0x5400
	v_mov_b32_e32 v4, s10
	v_mov_b32_e32 v5, 1
	s_waitcnt lgkmcnt(0)
	v_readfirstlane_b32 s12, v2
	v_readfirstlane_b32 s13, v3
	global_atomic_add v6, v4, v5, s[50:51] sc0
	s_add_u32 s14, s101, 1
	s_mul_i32 s15, s14, s12
	s_mul_i32 s16, s14, s13
	s_add_u32 s17, s9, 0x6400
	v_mov_b32_e32 v7, s17
	s_waitcnt vmcnt(0)
	v_readfirstlane_b32 s18, v6
	s_add_u32 s18, s18, 1
	s_cmp_lg_u32 s18, s15
	s_cbranch_scc1 .Lgb9_wait
	buffer_wbl2 sc1
	s_waitcnt vmcnt(0)
	v_mov_b32_e32 v8, 0x7400
	global_atomic_add v9, v8, v5, s[50:51] sc0
	s_waitcnt vmcnt(0)
	v_readfirstlane_b32 s19, v9
	s_add_u32 s19, s19, 1
	s_cmp_lg_u32 s19, s16
	s_cbranch_scc1 .Lgb9_wait
	v_mov_b32_e32 v8, 0x6400
	global_atomic_add v8, v5, s[50:51]
	global_atomic_add v8, v5, s[50:51] offset:256
	global_atomic_add v8, v5, s[50:51] offset:512
	global_atomic_add v8, v5, s[50:51] offset:768
	global_atomic_add v8, v5, s[50:51] offset:1024
	global_atomic_add v8, v5, s[50:51] offset:1280
	global_atomic_add v8, v5, s[50:51] offset:1536
	global_atomic_add v8, v5, s[50:51] offset:1792
	global_atomic_add v8, v5, s[50:51] offset:2048
	global_atomic_add v8, v5, s[50:51] offset:2304
	global_atomic_add v8, v5, s[50:51] offset:2560
	global_atomic_add v8, v5, s[50:51] offset:2816
	global_atomic_add v8, v5, s[50:51] offset:3072
	global_atomic_add v8, v5, s[50:51] offset:3328
	global_atomic_add v8, v5, s[50:51] offset:3584
	global_atomic_add v8, v5, s[50:51] offset:3840
	v_mov_b32_e32 v8, 0x7500
	global_atomic_add v8, v5, s[50:51]
	s_branch .Lgb9_acq

; __device__ __forceinline__ unsigned xb_ld(unsigned* p)              { return __hip_atomic_load(p, __ATOMIC_RELAXED, __HIP_MEMORY_SCOPE_AGENT); }
; __device__ __forceinline__ unsigned xb_add(unsigned* p, unsigned v) { return __hip_atomic_fetch_add(p, v, __ATOMIC_RELAXED, __HIP_MEMORY_SCOPE_AGENT); }
; #define XB_SPIN(cond, bar) do { unsigned _sp = 0; while (cond) { __builtin_amdgcn_s_sleep(1); \
;     if ((++_sp & 255u) == 0u) { if (xb_ld(&(bar)[XB_TMO])) break; if (_sp > XB_SPIN_CAP) { atomicAdd(&(bar)[XB_TMO], 1u); break; } } } } while (0)
; #define SEAM(k) do { if (IN(k) && IN((k) + 1)) GRID_BAR(); } while (0)
; __device__ __forceinline__ void xcd_barrier(const XcdBarrier& b) {
;     asm volatile("s_waitcnt vmcnt(0)" ::: "memory");
;     __syncthreads();
;     if (threadIdx.x == 0) {
;         unsigned* bar = b.bar;
;         __builtin_amdgcn_s_waitcnt(0);
;         unsigned nloc = b.st[0], nx = b.st[1];
;         if (nloc == 0u) { xcd_barrier_complete(bar, b.x, nloc, nx); b.st[0] = nloc; b.st[1] = nx; }
;         const unsigned old = xb_add(&bar[XB_XSUB(b.x)], 1u);
;         const unsigned gen = old / nloc;
;         if (old + 1u == (gen + 1u) * nloc) {
;             __builtin_amdgcn_fence(__ATOMIC_RELEASE, "agent");
;             asm volatile("s_waitcnt vmcnt(0)" ::: "memory");
;             const unsigned og = xb_add(&bar[XB_TOP], 1u);
;             const unsigned tg = og / nx;
;             if (og + 1u == (tg + 1u) * nx) xb_add(&bar[XB_TOPGEN], 1u);
;             else XB_SPIN(xb_ld(&bar[XB_TOPGEN]) == tg, bar);
;             __builtin_amdgcn_fence(__ATOMIC_ACQUIRE, "agent");
;             xb_add(&bar[XB_XGEN(b.x)], 1u);
;             asm volatile("s_waitcnt vmcnt(0)" ::: "memory");
;         } else {
;             XB_SPIN(xb_ld(&bar[XB_XGEN(b.x)]) == gen, bar);
;             __builtin_amdgcn_fence(__ATOMIC_ACQUIRE, "agent");
;             asm volatile("s_waitcnt vmcnt(0)" ::: "memory");
;         }
;     }
;     __syncthreads();
; }
; template <int L>
; __device__ __forceinline__ void layer(Frame& F, const XcdBarrier& bar, float* out, const int lo, const int hi) {
;     ...
;         SEAM(pb + 7);
.LBB0_1321:
	v_readlane_b32 s0, v255, 11
	v_readlane_b32 s1, v255, 12
	s_cmp_gt_i32 s1, 10
	s_cselect_b64 s[0:1], -1, 0
	s_and_b64 s[6:7], s[28:29], s[0:1]
	s_andn2_b64 vcc, exec, s[6:7]
	s_cbranch_vccnz .LBB0_1375
	s_waitcnt vmcnt(0)
	s_waitcnt vmcnt(0) lgkmcnt(0)
	s_barrier
	s_mov_b64 s[6:7], exec
	v_readlane_b32 s8, v255, 7
	v_readlane_b32 s9, v255, 8
	s_and_b64 s[8:9], s[6:7], s[8:9]
	s_mov_b64 exec, s[8:9]
	s_cbranch_execz .LBB0_1374
	s_add_i32 s3, 0, 0x20160
	v_mov_b32_e32 v1, s3
	ds_read_b64 v[2:3], v1
	v_readlane_b32 s8, v255, 6
	s_lshl_b32 s9, s8, 8
	s_add_u32 s10, s9, 0x5400
	v_mov_b32_e32 v4, s10
	v_mov_b32_e32 v5, 1
	s_waitcnt lgkmcnt(0)
	v_readfirstlane_b32 s12, v2
	v_readfirstlane_b32 s13, v3
	global_atomic_add v6, v4, v5, s[50:51] sc0
	s_add_u32 s14, s101, 1
	s_mul_i32 s15, s14, s12
	s_mul_i32 s16, s14, s13
	s_add_u32 s17, s9, 0x6400
	v_mov_b32_e32 v7, s17
	s_waitcnt vmcnt(0)
	v_readfirstlane_b32 s18, v6
	s_add_u32 s18, s18, 1
	s_cmp_lg_u32 s18, s15
	s_cbranch_scc1 .Lgb10_wait
	buffer_wbl2 sc1
	s_waitcnt vmcnt(0)
	v_mov_b32_e32 v8, 0x7400
	global_atomic_add v9, v8, v5, s[50:51] sc0
	s_waitcnt vmcnt(0)
	v_readfirstlane_b32 s19, v9
	s_add_u32 s19, s19, 1
	s_cmp_lg_u32 s19, s16
	s_cbranch_scc1 .Lgb10_wait
	v_mov_b32_e32 v8, 0x6400
	global_atomic_add v8, v5, s[50:51]
	global_atomic_add v8, v5, s[50:51] offset:256
	global_atomic_add v8, v5, s[50:51] offset:512
	global_atomic_add v8, v5, s[50:51] offset:768
	global_atomic_add v8, v5, s[50:51] offset:1024
	global_atomic_add v8, v5, s[50:51] offset:1280
	global_atomic_add v8, v5, s[50:51] offset:1536
	global_atomic_add v8, v5, s[50:51] offset:1792
	global_atomic_add v8, v5, s[50:51] offset:2048
	global_atomic_add v8, v5, s[50:51] offset:2304
	global_atomic_add v8, v5, s[50:51] offset:2560
	global_atomic_add v8, v5, s[50:51] offset:2816
	global_atomic_add v8, v5, s[50:51] offset:3072
	global_atomic_add v8, v5, s[50:51] offset:3328
	global_atomic_add v8, v5, s[50:51] offset:3584
	global_atomic_add v8, v5, s[50:51] offset:3840
	v_mov_b32_e32 v8, 0x7500
	global_atomic_add v8, v5, s[50:51]
	s_branch .Lgb10_acq

; __device__ __forceinline__ unsigned xb_ld(unsigned* p)              { return __hip_atomic_load(p, __ATOMIC_RELAXED, __HIP_MEMORY_SCOPE_AGENT); }
; __device__ __forceinline__ unsigned xb_add(unsigned* p, unsigned v) { return __hip_atomic_fetch_add(p, v, __ATOMIC_RELAXED, __HIP_MEMORY_SCOPE_AGENT); }
; #define XB_SPIN(cond, bar) do { unsigned _sp = 0; while (cond) { __builtin_amdgcn_s_sleep(1); \
;     if ((++_sp & 255u) == 0u) { if (xb_ld(&(bar)[XB_TMO])) break; if (_sp > XB_SPIN_CAP) { atomicAdd(&(bar)[XB_TMO], 1u); break; } } } } while (0)
; #define SEAM(k) do { if (IN(k) && IN((k) + 1)) GRID_BAR(); } while (0)
; __device__ __forceinline__ void xcd_barrier(const XcdBarrier& b) {
;     asm volatile("s_waitcnt vmcnt(0)" ::: "memory");
;     __syncthreads();
;     if (threadIdx.x == 0) {
;         unsigned* bar = b.bar;
;         __builtin_amdgcn_s_waitcnt(0);
;         unsigned nloc = b.st[0], nx = b.st[1];
;         if (nloc == 0u) { xcd_barrier_complete(bar, b.x, nloc, nx); b.st[0] = nloc; b.st[1] = nx; }
;         const unsigned old = xb_add(&bar[XB_XSUB(b.x)], 1u);
;         const unsigned gen = old / nloc;
;         if (old + 1u == (gen + 1u) * nloc) {
;             __builtin_amdgcn_fence(__ATOMIC_RELEASE, "agent");
;             asm volatile("s_waitcnt vmcnt(0)" ::: "memory");
;             const unsigned og = xb_add(&bar[XB_TOP], 1u);
;             const unsigned tg = og / nx;
;             if (og + 1u == (tg + 1u) * nx) xb_add(&bar[XB_TOPGEN], 1u);
;             else XB_SPIN(xb_ld(&bar[XB_TOPGEN]) == tg, bar);
;             __builtin_amdgcn_fence(__ATOMIC_ACQUIRE, "agent");
;             xb_add(&bar[XB_XGEN(b.x)], 1u);
;             asm volatile("s_waitcnt vmcnt(0)" ::: "memory");
;         } else {
;             XB_SPIN(xb_ld(&bar[XB_XGEN(b.x)]) == gen, bar);
;             __builtin_amdgcn_fence(__ATOMIC_ACQUIRE, "agent");
;             asm volatile("s_waitcnt vmcnt(0)" ::: "memory");
;         }
;     }
;     __syncthreads();
; }
; template <int L>
; __device__ __forceinline__ void layer(Frame& F, const XcdBarrier& bar, float* out, const int lo, const int hi) {
;     ...
;     SEAM(pb + 0);
.LBB0_1407:
	v_readlane_b32 s0, v255, 11
	v_readlane_b32 s1, v255, 12
	s_cmp_gt_i32 s1, 11
	s_cselect_b64 s[6:7], -1, 0
	s_and_b64 s[0:1], s[12:13], s[6:7]
	s_andn2_b64 vcc, exec, s[0:1]
	s_cbranch_vccnz .LBB0_1461
	s_waitcnt vmcnt(0)
	s_waitcnt vmcnt(0) lgkmcnt(0)
	s_barrier
	s_mov_b64 s[0:1], exec
	v_readlane_b32 s8, v255, 7
	v_readlane_b32 s9, v255, 8
	s_and_b64 s[8:9], s[0:1], s[8:9]
	s_mov_b64 exec, s[8:9]
	s_cbranch_execz .LBB0_1460
	s_add_i32 s3, 0, 0x20160
	v_mov_b32_e32 v1, s3
	ds_read_b64 v[2:3], v1
	v_readlane_b32 s8, v255, 6
	s_lshl_b32 s9, s8, 8
	s_add_u32 s10, s9, 0x5400
	v_mov_b32_e32 v4, s10
	v_mov_b32_e32 v5, 1
	s_waitcnt lgkmcnt(0)
	v_readfirstlane_b32 s12, v2
	v_readfirstlane_b32 s13, v3
	global_atomic_add v6, v4, v5, s[50:51] sc0
	s_add_u32 s14, s101, 1
	s_mul_i32 s15, s14, s12
	s_mul_i32 s16, s14, s13
	s_add_u32 s17, s9, 0x6400
	v_mov_b32_e32 v7, s17
	s_waitcnt vmcnt(0)
	v_readfirstlane_b32 s18, v6
	s_add_u32 s18, s18, 1
	s_cmp_lg_u32 s18, s15
	s_cbranch_scc1 .Lgb11_wait
	buffer_wbl2 sc1
	s_waitcnt vmcnt(0)
	v_mov_b32_e32 v8, 0x7400
	global_atomic_add v9, v8, v5, s[50:51] sc0
	s_waitcnt vmcnt(0)
	v_readfirstlane_b32 s19, v9
	s_add_u32 s19, s19, 1
	s_cmp_lg_u32 s19, s16
	s_cbranch_scc1 .Lgb11_wait
	v_mov_b32_e32 v8, 0x6400
	global_atomic_add v8, v5, s[50:51]
	global_atomic_add v8, v5, s[50:51] offset:256
	global_atomic_add v8, v5, s[50:51] offset:512
	global_atomic_add v8, v5, s[50:51] offset:768
	global_atomic_add v8, v5, s[50:51] offset:1024
	global_atomic_add v8, v5, s[50:51] offset:1280
	global_atomic_add v8, v5, s[50:51] offset:1536
	global_atomic_add v8, v5, s[50:51] offset:1792
	global_atomic_add v8, v5, s[50:51] offset:2048
	global_atomic_add v8, v5, s[50:51] offset:2304
	global_atomic_add v8, v5, s[50:51] offset:2560
	global_atomic_add v8, v5, s[50:51] offset:2816
	global_atomic_add v8, v5, s[50:51] offset:3072
	global_atomic_add v8, v5, s[50:51] offset:3328
	global_atomic_add v8, v5, s[50:51] offset:3584
	global_atomic_add v8, v5, s[50:51] offset:3840
	v_mov_b32_e32 v8, 0x7500
	global_atomic_add v8, v5, s[50:51]
	s_branch .Lgb11_acq

; __device__ __forceinline__ unsigned xb_ld(unsigned* p)              { return __hip_atomic_load(p, __ATOMIC_RELAXED, __HIP_MEMORY_SCOPE_AGENT); }
; __device__ __forceinline__ unsigned xb_add(unsigned* p, unsigned v) { return __hip_atomic_fetch_add(p, v, __ATOMIC_RELAXED, __HIP_MEMORY_SCOPE_AGENT); }
; #define XB_SPIN(cond, bar) do { unsigned _sp = 0; while (cond) { __builtin_amdgcn_s_sleep(1); \
;     if ((++_sp & 255u) == 0u) { if (xb_ld(&(bar)[XB_TMO])) break; if (_sp > XB_SPIN_CAP) { atomicAdd(&(bar)[XB_TMO], 1u); break; } } } } while (0)
; #define SEAM(k) do { if (IN(k) && IN((k) + 1)) GRID_BAR(); } while (0)
; __device__ __forceinline__ void xcd_barrier(const XcdBarrier& b) {
;     asm volatile("s_waitcnt vmcnt(0)" ::: "memory");
;     __syncthreads();
;     if (threadIdx.x == 0) {
;         unsigned* bar = b.bar;
;         __builtin_amdgcn_s_waitcnt(0);
;         unsigned nloc = b.st[0], nx = b.st[1];
;         if (nloc == 0u) { xcd_barrier_complete(bar, b.x, nloc, nx); b.st[0] = nloc; b.st[1] = nx; }
;         const unsigned old = xb_add(&bar[XB_XSUB(b.x)], 1u);
;         const unsigned gen = old / nloc;
;         if (old + 1u == (gen + 1u) * nloc) {
;             __builtin_amdgcn_fence(__ATOMIC_RELEASE, "agent");
;             asm volatile("s_waitcnt vmcnt(0)" ::: "memory");
;             const unsigned og = xb_add(&bar[XB_TOP], 1u);
;             const unsigned tg = og / nx;
;             if (og + 1u == (tg + 1u) * nx) xb_add(&bar[XB_TOPGEN], 1u);
;             else XB_SPIN(xb_ld(&bar[XB_TOPGEN]) == tg, bar);
;             __builtin_amdgcn_fence(__ATOMIC_ACQUIRE, "agent");
;             xb_add(&bar[XB_XGEN(b.x)], 1u);
;             asm volatile("s_waitcnt vmcnt(0)" ::: "memory");
;         } else {
;             XB_SPIN(xb_ld(&bar[XB_XGEN(b.x)]) == gen, bar);
;             __builtin_amdgcn_fence(__ATOMIC_ACQUIRE, "agent");
;             asm volatile("s_waitcnt vmcnt(0)" ::: "memory");
;         }
;     }
;     __syncthreads();
; }
; template <int L>
; __device__ __forceinline__ void layer(Frame& F, const XcdBarrier& bar, float* out, const int lo, const int hi) {
;     ...
;     SEAM(pb + 1);
.LBB0_1486:
	v_readlane_b32 s6, v255, 11
	v_readlane_b32 s7, v255, 12
	s_cmp_gt_i32 s7, 12
	s_cselect_b64 s[6:7], -1, 0
	s_and_b64 s[0:1], s[0:1], s[6:7]
	s_andn2_b64 vcc, exec, s[0:1]
	s_cbranch_vccnz .LBB0_1540
	s_waitcnt vmcnt(0)
	s_waitcnt vmcnt(0) lgkmcnt(0)
	s_barrier
	s_mov_b64 s[0:1], exec
	v_readlane_b32 s8, v255, 7
	v_readlane_b32 s9, v255, 8
	s_and_b64 s[8:9], s[0:1], s[8:9]
	s_mov_b64 exec, s[8:9]
	s_cbranch_execz .LBB0_1539
	s_add_i32 s3, 0, 0x20160
	v_mov_b32_e32 v1, s3
	ds_read_b64 v[2:3], v1
	v_readlane_b32 s8, v255, 6
	s_lshl_b32 s9, s8, 8
	s_add_u32 s10, s9, 0x5400
	v_mov_b32_e32 v4, s10
	v_mov_b32_e32 v5, 1
	s_waitcnt lgkmcnt(0)
	v_readfirstlane_b32 s12, v2
	v_readfirstlane_b32 s13, v3
	global_atomic_add v6, v4, v5, s[50:51] sc0
	s_add_u32 s14, s101, 1
	s_mul_i32 s15, s14, s12
	s_mul_i32 s16, s14, s13
	s_add_u32 s17, s9, 0x6400
	v_mov_b32_e32 v7, s17
	s_waitcnt vmcnt(0)
	v_readfirstlane_b32 s18, v6
	s_add_u32 s18, s18, 1
	s_cmp_lg_u32 s18, s15
	s_cbranch_scc1 .Lgb12_wait
	buffer_wbl2 sc1
	s_waitcnt vmcnt(0)
	v_mov_b32_e32 v8, 0x7400
	global_atomic_add v9, v8, v5, s[50:51] sc0
	s_waitcnt vmcnt(0)
	v_readfirstlane_b32 s19, v9
	s_add_u32 s19, s19, 1
	s_cmp_lg_u32 s19, s16
	s_cbranch_scc1 .Lgb12_wait
	v_mov_b32_e32 v8, 0x6400
	global_atomic_add v8, v5, s[50:51]
	global_atomic_add v8, v5, s[50:51] offset:256
	global_atomic_add v8, v5, s[50:51] offset:512
	global_atomic_add v8, v5, s[50:51] offset:768
	global_atomic_add v8, v5, s[50:51] offset:1024
	global_atomic_add v8, v5, s[50:51] offset:1280
	global_atomic_add v8, v5, s[50:51] offset:1536
	global_atomic_add v8, v5, s[50:51] offset:1792
	global_atomic_add v8, v5, s[50:51] offset:2048
	global_atomic_add v8, v5, s[50:51] offset:2304
	global_atomic_add v8, v5, s[50:51] offset:2560
	global_atomic_add v8, v5, s[50:51] offset:2816
	global_atomic_add v8, v5, s[50:51] offset:3072
	global_atomic_add v8, v5, s[50:51] offset:3328
	global_atomic_add v8, v5, s[50:51] offset:3584
	global_atomic_add v8, v5, s[50:51] offset:3840
	v_mov_b32_e32 v8, 0x7500
	global_atomic_add v8, v5, s[50:51]
	s_branch .Lgb12_acq

; __device__ __forceinline__ unsigned xb_ld(unsigned* p)              { return __hip_atomic_load(p, __ATOMIC_RELAXED, __HIP_MEMORY_SCOPE_AGENT); }
; __device__ __forceinline__ unsigned xb_add(unsigned* p, unsigned v) { return __hip_atomic_fetch_add(p, v, __ATOMIC_RELAXED, __HIP_MEMORY_SCOPE_AGENT); }
; #define XB_SPIN(cond, bar) do { unsigned _sp = 0; while (cond) { __builtin_amdgcn_s_sleep(1); \
;     if ((++_sp & 255u) == 0u) { if (xb_ld(&(bar)[XB_TMO])) break; if (_sp > XB_SPIN_CAP) { atomicAdd(&(bar)[XB_TMO], 1u); break; } } } } while (0)
; #define GRID_BAR() do { if (N_LAUNCHES == 1) xcd_barrier(bar); } while (0)
; __device__ __forceinline__ void xcd_barrier(const XcdBarrier& b) {
;     asm volatile("s_waitcnt vmcnt(0)" ::: "memory");
;     __syncthreads();
;     if (threadIdx.x == 0) {
;         unsigned* bar = b.bar;
;         __builtin_amdgcn_s_waitcnt(0);
;         unsigned nloc = b.st[0], nx = b.st[1];
;         if (nloc == 0u) { xcd_barrier_complete(bar, b.x, nloc, nx); b.st[0] = nloc; b.st[1] = nx; }
;         const unsigned old = xb_add(&bar[XB_XSUB(b.x)], 1u);
;         const unsigned gen = old / nloc;
;         if (old + 1u == (gen + 1u) * nloc) {
;             __builtin_amdgcn_fence(__ATOMIC_RELEASE, "agent");
;             asm volatile("s_waitcnt vmcnt(0)" ::: "memory");
;             const unsigned og = xb_add(&bar[XB_TOP], 1u);
;             const unsigned tg = og / nx;
;             if (og + 1u == (tg + 1u) * nx) xb_add(&bar[XB_TOPGEN], 1u);
;             else XB_SPIN(xb_ld(&bar[XB_TOPGEN]) == tg, bar);
;             __builtin_amdgcn_fence(__ATOMIC_ACQUIRE, "agent");
;             xb_add(&bar[XB_XGEN(b.x)], 1u);
;             asm volatile("s_waitcnt vmcnt(0)" ::: "memory");
;         } else {
;             XB_SPIN(xb_ld(&bar[XB_XGEN(b.x)]) == gen, bar);
;             __builtin_amdgcn_fence(__ATOMIC_ACQUIRE, "agent");
;             asm volatile("s_waitcnt vmcnt(0)" ::: "memory");
;         }
;     }
;     __syncthreads();
; }
; template <int L>
; __device__ __forceinline__ void layer(Frame& F, const XcdBarrier& bar, float* out, const int lo, const int hi) {
;     ...
;         GRID_BAR();
.LBB0_1617:
	s_waitcnt vmcnt(0)
	s_waitcnt vmcnt(0) lgkmcnt(0)
	s_barrier
	s_mov_b64 s[0:1], exec
	v_readlane_b32 s6, v255, 7
	v_readlane_b32 s7, v255, 8
	s_and_b64 s[6:7], s[0:1], s[6:7]
	s_mov_b64 exec, s[6:7]
	s_cbranch_execz .LBB0_1669
	s_add_i32 s3, 0, 0x20160
	v_mov_b32_e32 v1, s3
	ds_read_b64 v[2:3], v1
	v_readlane_b32 s8, v255, 6
	s_lshl_b32 s9, s8, 8
	s_add_u32 s10, s9, 0x5400
	v_mov_b32_e32 v4, s10
	v_mov_b32_e32 v5, 1
	s_waitcnt lgkmcnt(0)
	v_readfirstlane_b32 s12, v2
	v_readfirstlane_b32 s13, v3
	global_atomic_add v6, v4, v5, s[50:51] sc0
	s_add_u32 s14, s101, 1
	s_mul_i32 s15, s14, s12
	s_mul_i32 s16, s14, s13
	s_add_u32 s17, s9, 0x6400
	v_mov_b32_e32 v7, s17
	s_waitcnt vmcnt(0)
	v_readfirstlane_b32 s18, v6
	s_add_u32 s18, s18, 1
	s_cmp_lg_u32 s18, s15
	s_cbranch_scc1 .Lgb13_wait
	buffer_wbl2 sc1
	s_waitcnt vmcnt(0)
	v_mov_b32_e32 v8, 0x7400
	global_atomic_add v9, v8, v5, s[50:51] sc0
	s_waitcnt vmcnt(0)
	v_readfirstlane_b32 s19, v9
	s_add_u32 s19, s19, 1
	s_cmp_lg_u32 s19, s16
	s_cbranch_scc1 .Lgb13_wait
	v_mov_b32_e32 v8, 0x6400
	global_atomic_add v8, v5, s[50:51]
	global_atomic_add v8, v5, s[50:51] offset:256
	global_atomic_add v8, v5, s[50:51] offset:512
	global_atomic_add v8, v5, s[50:51] offset:768
	global_atomic_add v8, v5, s[50:51] offset:1024
	global_atomic_add v8, v5, s[50:51] offset:1280
	global_atomic_add v8, v5, s[50:51] offset:1536
	global_atomic_add v8, v5, s[50:51] offset:1792
	global_atomic_add v8, v5, s[50:51] offset:2048
	global_atomic_add v8, v5, s[50:51] offset:2304
	global_atomic_add v8, v5, s[50:51] offset:2560
	global_atomic_add v8, v5, s[50:51] offset:2816
	global_atomic_add v8, v5, s[50:51] offset:3072
	global_atomic_add v8, v5, s[50:51] offset:3328
	global_atomic_add v8, v5, s[50:51] offset:3584
	global_atomic_add v8, v5, s[50:51] offset:3840
	v_mov_b32_e32 v8, 0x7500
	global_atomic_add v8, v5, s[50:51]
	s_branch .Lgb13_acq

; __device__ __forceinline__ unsigned xb_ld(unsigned* p)              { return __hip_atomic_load(p, __ATOMIC_RELAXED, __HIP_MEMORY_SCOPE_AGENT); }
; __device__ __forceinline__ unsigned xb_add(unsigned* p, unsigned v) { return __hip_atomic_fetch_add(p, v, __ATOMIC_RELAXED, __HIP_MEMORY_SCOPE_AGENT); }
; #define XB_SPIN(cond, bar) do { unsigned _sp = 0; while (cond) { __builtin_amdgcn_s_sleep(1); \
;     if ((++_sp & 255u) == 0u) { if (xb_ld(&(bar)[XB_TMO])) break; if (_sp > XB_SPIN_CAP) { atomicAdd(&(bar)[XB_TMO], 1u); break; } } } } while (0)
; #define SEAM(k) do { if (IN(k) && IN((k) + 1)) GRID_BAR(); } while (0)
; __device__ __forceinline__ void xcd_barrier(const XcdBarrier& b) {
;     asm volatile("s_waitcnt vmcnt(0)" ::: "memory");
;     __syncthreads();
;     if (threadIdx.x == 0) {
;         unsigned* bar = b.bar;
;         __builtin_amdgcn_s_waitcnt(0);
;         unsigned nloc = b.st[0], nx = b.st[1];
;         if (nloc == 0u) { xcd_barrier_complete(bar, b.x, nloc, nx); b.st[0] = nloc; b.st[1] = nx; }
;         const unsigned old = xb_add(&bar[XB_XSUB(b.x)], 1u);
;         const unsigned gen = old / nloc;
;         if (old + 1u == (gen + 1u) * nloc) {
;             __builtin_amdgcn_fence(__ATOMIC_RELEASE, "agent");
;             asm volatile("s_waitcnt vmcnt(0)" ::: "memory");
;             const unsigned og = xb_add(&bar[XB_TOP], 1u);
;             const unsigned tg = og / nx;
;             if (og + 1u == (tg + 1u) * nx) xb_add(&bar[XB_TOPGEN], 1u);
;             else XB_SPIN(xb_ld(&bar[XB_TOPGEN]) == tg, bar);
;             __builtin_amdgcn_fence(__ATOMIC_ACQUIRE, "agent");
;             xb_add(&bar[XB_XGEN(b.x)], 1u);
;             asm volatile("s_waitcnt vmcnt(0)" ::: "memory");
;         } else {
;             XB_SPIN(xb_ld(&bar[XB_XGEN(b.x)]) == gen, bar);
;             __builtin_amdgcn_fence(__ATOMIC_ACQUIRE, "agent");
;             asm volatile("s_waitcnt vmcnt(0)" ::: "memory");
;         }
;     }
;     __syncthreads();
; }
; template <int L>
; __device__ __forceinline__ void layer(Frame& F, const XcdBarrier& bar, float* out, const int lo, const int hi) {
;     ...
;     SEAM(pb + 2);
.LBB0_2036:
	v_readlane_b32 s0, v255, 11
	v_readlane_b32 s1, v255, 12
	s_cmp_gt_i32 s1, 13
	v_readlane_b32 s0, v255, 37
	s_cselect_b64 s[6:7], -1, 0
	v_readlane_b32 s1, v255, 38
	s_and_b64 s[0:1], s[0:1], s[6:7]
	s_andn2_b64 vcc, exec, s[0:1]
	s_cbranch_vccnz .LBB0_2090
	s_waitcnt vmcnt(0)
	s_waitcnt vmcnt(0) lgkmcnt(0)
	s_barrier
	s_mov_b64 s[0:1], exec
	v_readlane_b32 s8, v255, 7
	v_readlane_b32 s9, v255, 8
	s_and_b64 s[8:9], s[0:1], s[8:9]
	s_mov_b64 exec, s[8:9]
	s_cbranch_execz .LBB0_2089
	s_add_i32 s3, 0, 0x20160
	v_mov_b32_e32 v1, s3
	ds_read_b64 v[2:3], v1
	v_readlane_b32 s8, v255, 6
	s_lshl_b32 s9, s8, 8
	s_add_u32 s10, s9, 0x5400
	v_mov_b32_e32 v4, s10
	v_mov_b32_e32 v5, 1
	s_waitcnt lgkmcnt(0)
	v_readfirstlane_b32 s12, v2
	v_readfirstlane_b32 s13, v3
	global_atomic_add v6, v4, v5, s[50:51] sc0
	s_add_u32 s14, s101, 1
	s_mul_i32 s15, s14, s12
	s_mul_i32 s16, s14, s13
	s_add_u32 s17, s9, 0x6400
	v_mov_b32_e32 v7, s17
	s_waitcnt vmcnt(0)
	v_readfirstlane_b32 s18, v6
	s_add_u32 s18, s18, 1
	s_cmp_lg_u32 s18, s15
	s_cbranch_scc1 .Lgb14_wait
	buffer_wbl2 sc1
	s_waitcnt vmcnt(0)
	v_mov_b32_e32 v8, 0x7400
	global_atomic_add v9, v8, v5, s[50:51] sc0
	s_waitcnt vmcnt(0)
	v_readfirstlane_b32 s19, v9
	s_add_u32 s19, s19, 1
	s_cmp_lg_u32 s19, s16
	s_cbranch_scc1 .Lgb14_wait
	v_mov_b32_e32 v8, 0x6400
	global_atomic_add v8, v5, s[50:51]
	global_atomic_add v8, v5, s[50:51] offset:256
	global_atomic_add v8, v5, s[50:51] offset:512
	global_atomic_add v8, v5, s[50:51] offset:768
	global_atomic_add v8, v5, s[50:51] offset:1024
	global_atomic_add v8, v5, s[50:51] offset:1280
	global_atomic_add v8, v5, s[50:51] offset:1536
	global_atomic_add v8, v5, s[50:51] offset:1792
	global_atomic_add v8, v5, s[50:51] offset:2048
	global_atomic_add v8, v5, s[50:51] offset:2304
	global_atomic_add v8, v5, s[50:51] offset:2560
	global_atomic_add v8, v5, s[50:51] offset:2816
	global_atomic_add v8, v5, s[50:51] offset:3072
	global_atomic_add v8, v5, s[50:51] offset:3328
	global_atomic_add v8, v5, s[50:51] offset:3584
	global_atomic_add v8, v5, s[50:51] offset:3840
	v_mov_b32_e32 v8, 0x7500
	global_atomic_add v8, v5, s[50:51]
	s_branch .Lgb14_acq

; __device__ __forceinline__ unsigned xb_ld(unsigned* p)              { return __hip_atomic_load(p, __ATOMIC_RELAXED, __HIP_MEMORY_SCOPE_AGENT); }
; __device__ __forceinline__ unsigned xb_add(unsigned* p, unsigned v) { return __hip_atomic_fetch_add(p, v, __ATOMIC_RELAXED, __HIP_MEMORY_SCOPE_AGENT); }
; #define XB_SPIN(cond, bar) do { unsigned _sp = 0; while (cond) { __builtin_amdgcn_s_sleep(1); \
;     if ((++_sp & 255u) == 0u) { if (xb_ld(&(bar)[XB_TMO])) break; if (_sp > XB_SPIN_CAP) { atomicAdd(&(bar)[XB_TMO], 1u); break; } } } } while (0)
; #define SEAM(k) do { if (IN(k) && IN((k) + 1)) GRID_BAR(); } while (0)
; __device__ __forceinline__ void xcd_barrier(const XcdBarrier& b) {
;     asm volatile("s_waitcnt vmcnt(0)" ::: "memory");
;     __syncthreads();
;     if (threadIdx.x == 0) {
;         unsigned* bar = b.bar;
;         __builtin_amdgcn_s_waitcnt(0);
;         unsigned nloc = b.st[0], nx = b.st[1];
;         if (nloc == 0u) { xcd_barrier_complete(bar, b.x, nloc, nx); b.st[0] = nloc; b.st[1] = nx; }
;         const unsigned old = xb_add(&bar[XB_XSUB(b.x)], 1u);
;         const unsigned gen = old / nloc;
;         if (old + 1u == (gen + 1u) * nloc) {
;             __builtin_amdgcn_fence(__ATOMIC_RELEASE, "agent");
;             asm volatile("s_waitcnt vmcnt(0)" ::: "memory");
;             const unsigned og = xb_add(&bar[XB_TOP], 1u);
;             const unsigned tg = og / nx;
;             if (og + 1u == (tg + 1u) * nx) xb_add(&bar[XB_TOPGEN], 1u);
;             else XB_SPIN(xb_ld(&bar[XB_TOPGEN]) == tg, bar);
;             __builtin_amdgcn_fence(__ATOMIC_ACQUIRE, "agent");
;             xb_add(&bar[XB_XGEN(b.x)], 1u);
;             asm volatile("s_waitcnt vmcnt(0)" ::: "memory");
;         } else {
;             XB_SPIN(xb_ld(&bar[XB_XGEN(b.x)]) == gen, bar);
;             __builtin_amdgcn_fence(__ATOMIC_ACQUIRE, "agent");
;             asm volatile("s_waitcnt vmcnt(0)" ::: "memory");
;         }
;     }
;     __syncthreads();
; }
; template <int L>
; __device__ __forceinline__ void layer(Frame& F, const XcdBarrier& bar, float* out, const int lo, const int hi) {
;     ...
;     SEAM(pb + 3);
.LBB0_2115:
	v_readlane_b32 s4, v255, 11
	v_readlane_b32 s5, v255, 12
	s_cmp_gt_i32 s5, 14
	s_cselect_b64 s[6:7], -1, 0
	s_and_b64 s[0:1], s[0:1], s[6:7]
	s_andn2_b64 vcc, exec, s[0:1]
	s_cbranch_vccnz .LBB0_2169
	s_waitcnt vmcnt(0)
	s_waitcnt vmcnt(0) lgkmcnt(0)
	s_barrier
	s_mov_b64 s[0:1], exec
	v_readlane_b32 s4, v255, 7
	v_readlane_b32 s5, v255, 8
	s_and_b64 s[4:5], s[0:1], s[4:5]
	s_mov_b64 exec, s[4:5]
	s_cbranch_execz .LBB0_2168
	s_add_i32 s3, 0, 0x20160
	v_mov_b32_e32 v1, s3
	ds_read_b64 v[2:3], v1
	v_readlane_b32 s8, v255, 6
	s_lshl_b32 s9, s8, 8
	s_add_u32 s10, s9, 0x5400
	v_mov_b32_e32 v4, s10
	v_mov_b32_e32 v5, 1
	s_waitcnt lgkmcnt(0)
	v_readfirstlane_b32 s12, v2
	v_readfirstlane_b32 s13, v3
	global_atomic_add v6, v4, v5, s[50:51] sc0
	s_add_u32 s14, s101, 1
	s_mul_i32 s15, s14, s12
	s_mul_i32 s16, s14, s13
	s_add_u32 s17, s9, 0x6400
	v_mov_b32_e32 v7, s17
	s_waitcnt vmcnt(0)
	v_readfirstlane_b32 s18, v6
	s_add_u32 s18, s18, 1
	s_cmp_lg_u32 s18, s15
	s_cbranch_scc1 .Lgb15_wait
	buffer_wbl2 sc1
	s_waitcnt vmcnt(0)
	v_mov_b32_e32 v8, 0x7400
	global_atomic_add v9, v8, v5, s[50:51] sc0
	s_waitcnt vmcnt(0)
	v_readfirstlane_b32 s19, v9
	s_add_u32 s19, s19, 1
	s_cmp_lg_u32 s19, s16
	s_cbranch_scc1 .Lgb15_wait
	v_mov_b32_e32 v8, 0x6400
	global_atomic_add v8, v5, s[50:51]
	global_atomic_add v8, v5, s[50:51] offset:256
	global_atomic_add v8, v5, s[50:51] offset:512
	global_atomic_add v8, v5, s[50:51] offset:768
	global_atomic_add v8, v5, s[50:51] offset:1024
	global_atomic_add v8, v5, s[50:51] offset:1280
	global_atomic_add v8, v5, s[50:51] offset:1536
	global_atomic_add v8, v5, s[50:51] offset:1792
	global_atomic_add v8, v5, s[50:51] offset:2048
	global_atomic_add v8, v5, s[50:51] offset:2304
	global_atomic_add v8, v5, s[50:51] offset:2560
	global_atomic_add v8, v5, s[50:51] offset:2816
	global_atomic_add v8, v5, s[50:51] offset:3072
	global_atomic_add v8, v5, s[50:51] offset:3328
	global_atomic_add v8, v5, s[50:51] offset:3584
	global_atomic_add v8, v5, s[50:51] offset:3840
	v_mov_b32_e32 v8, 0x7500
	global_atomic_add v8, v5, s[50:51]
	s_branch .Lgb15_acq

; __device__ __forceinline__ unsigned xb_ld(unsigned* p)              { return __hip_atomic_load(p, __ATOMIC_RELAXED, __HIP_MEMORY_SCOPE_AGENT); }
; __device__ __forceinline__ unsigned xb_add(unsigned* p, unsigned v) { return __hip_atomic_fetch_add(p, v, __ATOMIC_RELAXED, __HIP_MEMORY_SCOPE_AGENT); }
; #define XB_SPIN(cond, bar) do { unsigned _sp = 0; while (cond) { __builtin_amdgcn_s_sleep(1); \
;     if ((++_sp & 255u) == 0u) { if (xb_ld(&(bar)[XB_TMO])) break; if (_sp > XB_SPIN_CAP) { atomicAdd(&(bar)[XB_TMO], 1u); break; } } } } while (0)
; #define SEAM(k) do { if (IN(k) && IN((k) + 1)) GRID_BAR(); } while (0)
; __device__ __forceinline__ void xcd_barrier(const XcdBarrier& b) {
;     asm volatile("s_waitcnt vmcnt(0)" ::: "memory");
;     __syncthreads();
;     if (threadIdx.x == 0) {
;         unsigned* bar = b.bar;
;         __builtin_amdgcn_s_waitcnt(0);
;         unsigned nloc = b.st[0], nx = b.st[1];
;         if (nloc == 0u) { xcd_barrier_complete(bar, b.x, nloc, nx); b.st[0] = nloc; b.st[1] = nx; }
;         const unsigned old = xb_add(&bar[XB_XSUB(b.x)], 1u);
;         const unsigned gen = old / nloc;
;         if (old + 1u == (gen + 1u) * nloc) {
;             __builtin_amdgcn_fence(__ATOMIC_RELEASE, "agent");
;             asm volatile("s_waitcnt vmcnt(0)" ::: "memory");
;             const unsigned og = xb_add(&bar[XB_TOP], 1u);
;             const unsigned tg = og / nx;
;             if (og + 1u == (tg + 1u) * nx) xb_add(&bar[XB_TOPGEN], 1u);
;             else XB_SPIN(xb_ld(&bar[XB_TOPGEN]) == tg, bar);
;             __builtin_amdgcn_fence(__ATOMIC_ACQUIRE, "agent");
;             xb_add(&bar[XB_XGEN(b.x)], 1u);
;             asm volatile("s_waitcnt vmcnt(0)" ::: "memory");
;         } else {
;             XB_SPIN(xb_ld(&bar[XB_XGEN(b.x)]) == gen, bar);
;             __builtin_amdgcn_fence(__ATOMIC_ACQUIRE, "agent");
;             asm volatile("s_waitcnt vmcnt(0)" ::: "memory");
;         }
;     }
;     __syncthreads();
; }
; template <int L>
; __device__ __forceinline__ void layer(Frame& F, const XcdBarrier& bar, float* out, const int lo, const int hi) {
;     ...
;     SEAM(pb + 4);
.LBB0_2198:
	v_readlane_b32 s0, v255, 11
	v_readlane_b32 s1, v255, 12
	s_cmp_gt_i32 s1, 15
	s_cselect_b64 s[6:7], -1, 0
	s_and_b64 s[0:1], s[12:13], s[6:7]
	s_andn2_b64 vcc, exec, s[0:1]
	s_cbranch_vccnz .LBB0_2252
	s_waitcnt vmcnt(0)
	s_waitcnt vmcnt(0) lgkmcnt(0)
	s_barrier
	s_mov_b64 s[0:1], exec
	v_readlane_b32 s4, v255, 7
	v_readlane_b32 s5, v255, 8
	s_and_b64 s[4:5], s[0:1], s[4:5]
	s_mov_b64 exec, s[4:5]
	s_cbranch_execz .LBB0_2251
	s_add_i32 s3, 0, 0x20160
	v_mov_b32_e32 v1, s3
	ds_read_b64 v[2:3], v1
	v_readlane_b32 s8, v255, 6
	s_lshl_b32 s9, s8, 8
	s_add_u32 s10, s9, 0x5400
	v_mov_b32_e32 v4, s10
	v_mov_b32_e32 v5, 1
	s_waitcnt lgkmcnt(0)
	v_readfirstlane_b32 s12, v2
	v_readfirstlane_b32 s13, v3
	global_atomic_add v6, v4, v5, s[50:51] sc0
	s_add_u32 s14, s101, 1
	s_mul_i32 s15, s14, s12
	s_mul_i32 s16, s14, s13
	s_add_u32 s17, s9, 0x6400
	v_mov_b32_e32 v7, s17
	s_waitcnt vmcnt(0)
	v_readfirstlane_b32 s18, v6
	s_add_u32 s18, s18, 1
	s_cmp_lg_u32 s18, s15
	s_cbranch_scc1 .Lgb16_wait
	buffer_wbl2 sc1
	s_waitcnt vmcnt(0)
	v_mov_b32_e32 v8, 0x7400
	global_atomic_add v9, v8, v5, s[50:51] sc0
	s_waitcnt vmcnt(0)
	v_readfirstlane_b32 s19, v9
	s_add_u32 s19, s19, 1
	s_cmp_lg_u32 s19, s16
	s_cbranch_scc1 .Lgb16_wait
	v_mov_b32_e32 v8, 0x6400
	global_atomic_add v8, v5, s[50:51]
	global_atomic_add v8, v5, s[50:51] offset:256
	global_atomic_add v8, v5, s[50:51] offset:512
	global_atomic_add v8, v5, s[50:51] offset:768
	global_atomic_add v8, v5, s[50:51] offset:1024
	global_atomic_add v8, v5, s[50:51] offset:1280
	global_atomic_add v8, v5, s[50:51] offset:1536
	global_atomic_add v8, v5, s[50:51] offset:1792
	global_atomic_add v8, v5, s[50:51] offset:2048
	global_atomic_add v8, v5, s[50:51] offset:2304
	global_atomic_add v8, v5, s[50:51] offset:2560
	global_atomic_add v8, v5, s[50:51] offset:2816
	global_atomic_add v8, v5, s[50:51] offset:3072
	global_atomic_add v8, v5, s[50:51] offset:3328
	global_atomic_add v8, v5, s[50:51] offset:3584
	global_atomic_add v8, v5, s[50:51] offset:3840
	v_mov_b32_e32 v8, 0x7500
	global_atomic_add v8, v5, s[50:51]
	s_branch .Lgb16_acq

; __device__ __forceinline__ unsigned xb_ld(unsigned* p)              { return __hip_atomic_load(p, __ATOMIC_RELAXED, __HIP_MEMORY_SCOPE_AGENT); }
; __device__ __forceinline__ unsigned xb_add(unsigned* p, unsigned v) { return __hip_atomic_fetch_add(p, v, __ATOMIC_RELAXED, __HIP_MEMORY_SCOPE_AGENT); }
; #define XB_SPIN(cond, bar) do { unsigned _sp = 0; while (cond) { __builtin_amdgcn_s_sleep(1); \
;     if ((++_sp & 255u) == 0u) { if (xb_ld(&(bar)[XB_TMO])) break; if (_sp > XB_SPIN_CAP) { atomicAdd(&(bar)[XB_TMO], 1u); break; } } } } while (0)
; #define SEAM(k) do { if (IN(k) && IN((k) + 1)) GRID_BAR(); } while (0)
; __device__ __forceinline__ void xcd_barrier(const XcdBarrier& b) {
;     asm volatile("s_waitcnt vmcnt(0)" ::: "memory");
;     __syncthreads();
;     if (threadIdx.x == 0) {
;         unsigned* bar = b.bar;
;         __builtin_amdgcn_s_waitcnt(0);
;         unsigned nloc = b.st[0], nx = b.st[1];
;         if (nloc == 0u) { xcd_barrier_complete(bar, b.x, nloc, nx); b.st[0] = nloc; b.st[1] = nx; }
;         const unsigned old = xb_add(&bar[XB_XSUB(b.x)], 1u);
;         const unsigned gen = old / nloc;
;         if (old + 1u == (gen + 1u) * nloc) {
;             __builtin_amdgcn_fence(__ATOMIC_RELEASE, "agent");
;             asm volatile("s_waitcnt vmcnt(0)" ::: "memory");
;             const unsigned og = xb_add(&bar[XB_TOP], 1u);
;             const unsigned tg = og / nx;
;             if (og + 1u == (tg + 1u) * nx) xb_add(&bar[XB_TOPGEN], 1u);
;             else XB_SPIN(xb_ld(&bar[XB_TOPGEN]) == tg, bar);
;             __builtin_amdgcn_fence(__ATOMIC_ACQUIRE, "agent");
;             xb_add(&bar[XB_XGEN(b.x)], 1u);
;             asm volatile("s_waitcnt vmcnt(0)" ::: "memory");
;         } else {
;             XB_SPIN(xb_ld(&bar[XB_XGEN(b.x)]) == gen, bar);
;             __builtin_amdgcn_fence(__ATOMIC_ACQUIRE, "agent");
;             asm volatile("s_waitcnt vmcnt(0)" ::: "memory");
;         }
;     }
;     __syncthreads();
; }
; template <int L>
; __device__ __forceinline__ void layer(Frame& F, const XcdBarrier& bar, float* out, const int lo, const int hi) {
;     ...
;         SEAM(pb + 5);
.LBB0_2317:
	v_readlane_b32 s4, v255, 11
	v_readlane_b32 s5, v255, 12
	s_cmp_gt_i32 s5, 16
	s_cselect_b64 s[6:7], -1, 0
	s_and_b64 s[0:1], s[0:1], s[6:7]
	s_andn2_b64 vcc, exec, s[0:1]
	s_cbranch_vccnz .LBB0_2371
	s_waitcnt vmcnt(0)
	s_waitcnt vmcnt(0) lgkmcnt(0)
	s_barrier
	s_mov_b64 s[0:1], exec
	v_readlane_b32 s4, v255, 7
	v_readlane_b32 s5, v255, 8
	s_and_b64 s[4:5], s[0:1], s[4:5]
	s_mov_b64 exec, s[4:5]
	s_cbranch_execz .LBB0_2370
	s_add_i32 s3, 0, 0x20160
	v_mov_b32_e32 v1, s3
	ds_read_b64 v[2:3], v1
	v_readlane_b32 s8, v255, 6
	s_lshl_b32 s9, s8, 8
	s_add_u32 s10, s9, 0x5400
	v_mov_b32_e32 v4, s10
	v_mov_b32_e32 v5, 1
	s_waitcnt lgkmcnt(0)
	v_readfirstlane_b32 s12, v2
	v_readfirstlane_b32 s13, v3
	global_atomic_add v6, v4, v5, s[50:51] sc0
	s_add_u32 s14, s101, 1
	s_mul_i32 s15, s14, s12
	s_mul_i32 s16, s14, s13
	s_add_u32 s17, s9, 0x6400
	v_mov_b32_e32 v7, s17
	s_waitcnt vmcnt(0)
	v_readfirstlane_b32 s18, v6
	s_add_u32 s18, s18, 1
	s_cmp_lg_u32 s18, s15
	s_cbranch_scc1 .Lgb17_wait
	buffer_wbl2 sc1
	s_waitcnt vmcnt(0)
	v_mov_b32_e32 v8, 0x7400
	global_atomic_add v9, v8, v5, s[50:51] sc0
	s_waitcnt vmcnt(0)
	v_readfirstlane_b32 s19, v9
	s_add_u32 s19, s19, 1
	s_cmp_lg_u32 s19, s16
	s_cbranch_scc1 .Lgb17_wait
	v_mov_b32_e32 v8, 0x6400
	global_atomic_add v8, v5, s[50:51]
	global_atomic_add v8, v5, s[50:51] offset:256
	global_atomic_add v8, v5, s[50:51] offset:512
	global_atomic_add v8, v5, s[50:51] offset:768
	global_atomic_add v8, v5, s[50:51] offset:1024
	global_atomic_add v8, v5, s[50:51] offset:1280
	global_atomic_add v8, v5, s[50:51] offset:1536
	global_atomic_add v8, v5, s[50:51] offset:1792
	global_atomic_add v8, v5, s[50:51] offset:2048
	global_atomic_add v8, v5, s[50:51] offset:2304
	global_atomic_add v8, v5, s[50:51] offset:2560
	global_atomic_add v8, v5, s[50:51] offset:2816
	global_atomic_add v8, v5, s[50:51] offset:3072
	global_atomic_add v8, v5, s[50:51] offset:3328
	global_atomic_add v8, v5, s[50:51] offset:3584
	global_atomic_add v8, v5, s[50:51] offset:3840
	v_mov_b32_e32 v8, 0x7500
	global_atomic_add v8, v5, s[50:51]
	s_branch .Lgb17_acq

; __device__ __forceinline__ unsigned xb_ld(unsigned* p)              { return __hip_atomic_load(p, __ATOMIC_RELAXED, __HIP_MEMORY_SCOPE_AGENT); }
; __device__ __forceinline__ unsigned xb_add(unsigned* p, unsigned v) { return __hip_atomic_fetch_add(p, v, __ATOMIC_RELAXED, __HIP_MEMORY_SCOPE_AGENT); }
; #define XB_SPIN(cond, bar) do { unsigned _sp = 0; while (cond) { __builtin_amdgcn_s_sleep(1); \
;     if ((++_sp & 255u) == 0u) { if (xb_ld(&(bar)[XB_TMO])) break; if (_sp > XB_SPIN_CAP) { atomicAdd(&(bar)[XB_TMO], 1u); break; } } } } while (0)
; #define SEAM(k) do { if (IN(k) && IN((k) + 1)) GRID_BAR(); } while (0)
; __device__ __forceinline__ void xcd_barrier(const XcdBarrier& b) {
;     asm volatile("s_waitcnt vmcnt(0)" ::: "memory");
;     __syncthreads();
;     if (threadIdx.x == 0) {
;         unsigned* bar = b.bar;
;         __builtin_amdgcn_s_waitcnt(0);
;         unsigned nloc = b.st[0], nx = b.st[1];
;         if (nloc == 0u) { xcd_barrier_complete(bar, b.x, nloc, nx); b.st[0] = nloc; b.st[1] = nx; }
;         const unsigned old = xb_add(&bar[XB_XSUB(b.x)], 1u);
;         const unsigned gen = old / nloc;
;         if (old + 1u == (gen + 1u) * nloc) {
;             __builtin_amdgcn_fence(__ATOMIC_RELEASE, "agent");
;             asm volatile("s_waitcnt vmcnt(0)" ::: "memory");
;             const unsigned og = xb_add(&bar[XB_TOP], 1u);
;             const unsigned tg = og / nx;
;             if (og + 1u == (tg + 1u) * nx) xb_add(&bar[XB_TOPGEN], 1u);
;             else XB_SPIN(xb_ld(&bar[XB_TOPGEN]) == tg, bar);
;             __builtin_amdgcn_fence(__ATOMIC_ACQUIRE, "agent");
;             xb_add(&bar[XB_XGEN(b.x)], 1u);
;             asm volatile("s_waitcnt vmcnt(0)" ::: "memory");
;         } else {
;             XB_SPIN(xb_ld(&bar[XB_XGEN(b.x)]) == gen, bar);
;             __builtin_amdgcn_fence(__ATOMIC_ACQUIRE, "agent");
;             asm volatile("s_waitcnt vmcnt(0)" ::: "memory");
;         }
;     }
;     __syncthreads();
; }
; template <int L>
; __device__ __forceinline__ void layer(Frame& F, const XcdBarrier& bar, float* out, const int lo, const int hi) {
;     ...
;         SEAM(pb + 6);
.LBB0_2394:
	v_readlane_b32 s4, v255, 11
	v_readlane_b32 s5, v255, 12
	s_cmp_gt_i32 s5, 17
	s_cselect_b64 s[6:7], -1, 0
	s_and_b64 s[0:1], s[0:1], s[6:7]
	s_andn2_b64 vcc, exec, s[0:1]
	s_cbranch_vccnz .LBB0_2448
	s_waitcnt vmcnt(0)
	s_waitcnt vmcnt(0) lgkmcnt(0)
	s_barrier
	s_mov_b64 s[0:1], exec
	v_readlane_b32 s4, v255, 7
	v_readlane_b32 s5, v255, 8
	s_and_b64 s[4:5], s[0:1], s[4:5]
	s_mov_b64 exec, s[4:5]
	s_cbranch_execz .LBB0_2447
	s_add_i32 s3, 0, 0x20160
	v_mov_b32_e32 v1, s3
	ds_read_b64 v[2:3], v1
	v_readlane_b32 s8, v255, 6
	s_lshl_b32 s9, s8, 8
	s_add_u32 s10, s9, 0x5400
	v_mov_b32_e32 v4, s10
	v_mov_b32_e32 v5, 1
	s_waitcnt lgkmcnt(0)
	v_readfirstlane_b32 s12, v2
	v_readfirstlane_b32 s13, v3
	global_atomic_add v6, v4, v5, s[50:51] sc0
	s_add_u32 s14, s101, 1
	s_mul_i32 s15, s14, s12
	s_mul_i32 s16, s14, s13
	s_add_u32 s17, s9, 0x6400
	v_mov_b32_e32 v7, s17
	s_waitcnt vmcnt(0)
	v_readfirstlane_b32 s18, v6
	s_add_u32 s18, s18, 1
	s_cmp_lg_u32 s18, s15
	s_cbranch_scc1 .Lgb18_wait
	buffer_wbl2 sc1
	s_waitcnt vmcnt(0)
	v_mov_b32_e32 v8, 0x7400
	global_atomic_add v9, v8, v5, s[50:51] sc0
	s_waitcnt vmcnt(0)
	v_readfirstlane_b32 s19, v9
	s_add_u32 s19, s19, 1
	s_cmp_lg_u32 s19, s16
	s_cbranch_scc1 .Lgb18_wait
	v_mov_b32_e32 v8, 0x6400
	global_atomic_add v8, v5, s[50:51]
	global_atomic_add v8, v5, s[50:51] offset:256
	global_atomic_add v8, v5, s[50:51] offset:512
	global_atomic_add v8, v5, s[50:51] offset:768
	global_atomic_add v8, v5, s[50:51] offset:1024
	global_atomic_add v8, v5, s[50:51] offset:1280
	global_atomic_add v8, v5, s[50:51] offset:1536
	global_atomic_add v8, v5, s[50:51] offset:1792
	global_atomic_add v8, v5, s[50:51] offset:2048
	global_atomic_add v8, v5, s[50:51] offset:2304
	global_atomic_add v8, v5, s[50:51] offset:2560
	global_atomic_add v8, v5, s[50:51] offset:2816
	global_atomic_add v8, v5, s[50:51] offset:3072
	global_atomic_add v8, v5, s[50:51] offset:3328
	global_atomic_add v8, v5, s[50:51] offset:3584
	global_atomic_add v8, v5, s[50:51] offset:3840
	v_mov_b32_e32 v8, 0x7500
	global_atomic_add v8, v5, s[50:51]
	s_branch .Lgb18_acq

; __global__ void __launch_bounds__(NTHR, 2) fwd(Args args) {
	.amdhsa_kernel _Z3fwd4Args
		.amdhsa_group_segment_fixed_size 0
		.amdhsa_private_segment_fixed_size 0
		.amdhsa_kernarg_size 464
		.amdhsa_user_sgpr_count 2
		.amdhsa_user_sgpr_dispatch_ptr 0
		.amdhsa_user_sgpr_queue_ptr 0
		.amdhsa_user_sgpr_kernarg_segment_ptr 1
		.amdhsa_user_sgpr_dispatch_id 0
		.amdhsa_user_sgpr_kernarg_preload_length 0
		.amdhsa_user_sgpr_kernarg_preload_offset 0
		.amdhsa_user_sgpr_private_segment_size 0
		.amdhsa_uses_dynamic_stack 0
		.amdhsa_enable_private_segment 0
		.amdhsa_system_sgpr_workgroup_id_x 1
		.amdhsa_system_sgpr_workgroup_id_y 0
		.amdhsa_system_sgpr_workgroup_id_z 0
		.amdhsa_system_sgpr_workgroup_info 0
		.amdhsa_system_vgpr_workitem_id 0
		.amdhsa_next_free_vgpr 256
		.amdhsa_next_free_sgpr 102
		.amdhsa_accum_offset 256
		.amdhsa_reserve_vcc 1
		.amdhsa_float_round_mode_32 0
		.amdhsa_float_round_mode_16_64 0
		.amdhsa_float_denorm_mode_32 3
		.amdhsa_float_denorm_mode_16_64 3
		.amdhsa_dx10_clamp 1
		.amdhsa_ieee_mode 1
		.amdhsa_fp16_overflow 0
		.amdhsa_tg_split 0
		.amdhsa_exception_fp_ieee_invalid_op 0
		.amdhsa_exception_fp_denorm_src 0
		.amdhsa_exception_fp_ieee_div_zero 0
		.amdhsa_exception_fp_ieee_overflow 0
		.amdhsa_exception_fp_ieee_underflow 0
		.amdhsa_exception_fp_ieee_inexact 0
		.amdhsa_exception_int_div_zero 0
	.end_amdhsa_kernel

; __global__ void __launch_bounds__(NTHR, 2) fwd(Args args) {
amdhsa.kernels:
  - .agpr_count:     0
    .args:
      - .offset:         0
        .size:           208
        .value_kind:     by_value
      - .offset:         208
        .size:           4
        .value_kind:     hidden_block_count_x
      - .offset:         212
        .size:           4
        .value_kind:     hidden_block_count_y
      - .offset:         216
        .size:           4
        .value_kind:     hidden_block_count_z
      - .offset:         220
        .size:           2
        .value_kind:     hidden_group_size_x
      - .offset:         222
        .size:           2
        .value_kind:     hidden_group_size_y
      - .offset:         224
        .size:           2
        .value_kind:     hidden_group_size_z
      - .offset:         226
        .size:           2
        .value_kind:     hidden_remainder_x
      - .offset:         228
        .size:           2
        .value_kind:     hidden_remainder_y
      - .offset:         230
        .size:           2
        .value_kind:     hidden_remainder_z
      - .offset:         248
        .size:           8
        .value_kind:     hidden_global_offset_x
      - .offset:         256
        .size:           8
        .value_kind:     hidden_global_offset_y
      - .offset:         264
        .size:           8
        .value_kind:     hidden_global_offset_z
      - .offset:         272
        .size:           2
        .value_kind:     hidden_grid_dims
      - .offset:         328
        .size:           4
        .value_kind:     hidden_dynamic_lds_size
    .group_segment_fixed_size: 0
    .kernarg_segment_align: 8
    .kernarg_segment_size: 464
    .language:       OpenCL C
    .language_version:
      - 2
      - 0
    .max_flat_workgroup_size: 512
    .name:           _Z3fwd4Args
    .private_segment_fixed_size: 0
    .sgpr_count:     108
    .sgpr_spill_count: 80
    .symbol:         _Z3fwd4Args.kd
    .uniform_work_group_size: 1
    .uses_dynamic_stack: false
    .vgpr_count:     256
    .vgpr_spill_count: 0
    .wavefront_size: 64
